# RG-LRU scan unit rewritten by hand: thread = 4 channels x 17 positions, 16-byte/8-byte global accesses, branch-free addresses, in-wave bpermute scan + 8-entry cross-wave fold for the chunk carries (f3
# speedup vs baseline: 1.0094x; 1.0094x over previous
.LBB0_460:
	s_or_b64 exec, exec, s[0:1]
	v_readlane_b32 s0, v255, 33
	s_waitcnt lgkmcnt(0)
	s_barrier
	v_mov_b32_e32 v0, s0
	ds_read_b32 v0, v0
	s_movk_i32 s0, 0x10f
	s_waitcnt lgkmcnt(0)
	s_barrier
	v_cmp_lt_i32_e32 vcc, s0, v0
	v_readfirstlane_b32 s22, v0
	s_mov_b64 s[0:1], -1
	s_cbranch_vccnz .LBB0_455
	s_cmp_gt_i32 s22, 15
	s_cbranch_scc0 .LBB0_745
	s_add_i32 s0, s22, -16
	s_lshr_b32 s1, s0, 6
	s_and_b32 s0, s0, 63
	s_lshl_b32 s23, s0, 3
	s_lshl_b32 s26, s1, 12
	s_lshl_b32 s27, s1, 8
	s_or_b32 s27, s27, 0x4000
	v_mbcnt_lo_u32_b32 v0, -1, 0
	v_mbcnt_hi_u32_b32 v0, -1, v0
	v_readlane_b32 s0, v254, 27
	v_mov_b32_e32 v1, v0
	v_add_u32_e32 v0, s0, v0
	s_lshr_b32 s12, s0, 6
	v_and_b32_e32 v2, 1, v0
	v_lshrrev_b32_e32 v4, 1, v0
	v_mul_u32_u24_e32 v4, 17, v4
	v_lshl_add_u32 v5, v2, 2, s23
	v_lshlrev_b32_e32 v5, 2, v5
	v_lshlrev_b32_e32 v7, 2, v1
	v_sub_u32_e32 v6, 0x100, v4
	v_max_i32_e32 v6, 0, v6
	v_lshlrev_b32_e32 v8, 5, v2
	v_lshrrev_b32_e32 v15, 1, v5
	v_sub_u32_e32 v15, 0x400, v15
	s_movk_i32 s14, 0x1400
	s_add_u32 s8, s18, 0x2200000
	s_addc_u32 s9, s19, 0
	s_add_u32 s10, s20, 0x1100000
	s_addc_u32 s11, s21, 0
	s_addk_i32 s27, 0xff
	s_add_i32 s13, s26, 0x10ff
	v_sub_u32_e32 v9, s27, v4
	v_sub_u32_e32 v10, s13, v4
	s_addk_i32 s27, 0xff01
	v_lshl_add_u32 v11, v9, 11, v5
	v_lshl_add_u32 v12, v10, 11, v5
	v_cmp_lt_u32_e32 vcc, 0, v6
	v_cmp_lt_u32_e64 s[36:37], 1, v6
	s_nop 0
	v_cndmask_b32_e32 v248, v12, v11, vcc
	v_cndmask_b32_e64 v249, v12, v11, s[36:37]
	v_add_u32_e32 v249, 0xfffff800, v249
	global_load_dwordx4 v[16:19], v248, s[8:9]
	v_lshrrev_b32_e32 v250, 1, v248
	global_load_dwordx2 v[84:85], v250, s[10:11]
	global_load_dwordx4 v[20:23], v249, s[8:9]
	v_lshrrev_b32_e32 v250, 1, v249
	global_load_dwordx2 v[86:87], v250, s[10:11]
	v_cmp_lt_u32_e32 vcc, 2, v6
	v_cmp_lt_u32_e64 s[36:37], 3, v6
	s_nop 0
	v_cndmask_b32_e32 v248, v12, v11, vcc
	v_cndmask_b32_e64 v249, v12, v11, s[36:37]
	v_add_u32_e32 v248, 0xfffff000, v248
	v_add_u32_e32 v249, 0xffffe800, v249
	global_load_dwordx4 v[24:27], v248, s[8:9]
	v_lshrrev_b32_e32 v250, 1, v248
	global_load_dwordx2 v[88:89], v250, s[10:11]
	global_load_dwordx4 v[28:31], v249, s[8:9]
	v_lshrrev_b32_e32 v250, 1, v249
	global_load_dwordx2 v[90:91], v250, s[10:11]
	v_cmp_lt_u32_e32 vcc, 4, v6
	v_cmp_lt_u32_e64 s[36:37], 5, v6
	s_nop 0
	v_cndmask_b32_e32 v248, v12, v11, vcc
	v_cndmask_b32_e64 v249, v12, v11, s[36:37]
	v_add_u32_e32 v248, 0xffffe000, v248
	v_add_u32_e32 v249, 0xffffd800, v249
	global_load_dwordx4 v[32:35], v248, s[8:9]
	v_lshrrev_b32_e32 v250, 1, v248
	global_load_dwordx2 v[92:93], v250, s[10:11]
	global_load_dwordx4 v[36:39], v249, s[8:9]
	v_lshrrev_b32_e32 v250, 1, v249
	global_load_dwordx2 v[94:95], v250, s[10:11]
	v_cmp_lt_u32_e32 vcc, 6, v6
	v_cmp_lt_u32_e64 s[36:37], 7, v6
	s_nop 0
	v_cndmask_b32_e32 v248, v12, v11, vcc
	v_cndmask_b32_e64 v249, v12, v11, s[36:37]
	v_add_u32_e32 v248, 0xffffd000, v248
	v_add_u32_e32 v249, 0xffffc800, v249
	global_load_dwordx4 v[40:43], v248, s[8:9]
	v_lshrrev_b32_e32 v250, 1, v248
	global_load_dwordx2 v[96:97], v250, s[10:11]
	global_load_dwordx4 v[44:47], v249, s[8:9]
	v_lshrrev_b32_e32 v250, 1, v249
	global_load_dwordx2 v[98:99], v250, s[10:11]
	v_cmp_lt_u32_e32 vcc, 8, v6
	v_cmp_lt_u32_e64 s[36:37], 9, v6
	s_nop 0
	v_cndmask_b32_e32 v248, v12, v11, vcc
	v_cndmask_b32_e64 v249, v12, v11, s[36:37]
	v_add_u32_e32 v248, 0xffffc000, v248
	v_add_u32_e32 v249, 0xffffb800, v249
	global_load_dwordx4 v[48:51], v248, s[8:9]
	v_lshrrev_b32_e32 v250, 1, v248
	global_load_dwordx2 v[100:101], v250, s[10:11]
	global_load_dwordx4 v[52:55], v249, s[8:9]
	v_lshrrev_b32_e32 v250, 1, v249
	global_load_dwordx2 v[102:103], v250, s[10:11]
	v_cmp_lt_u32_e32 vcc, 10, v6
	v_cmp_lt_u32_e64 s[36:37], 11, v6
	s_nop 0
	v_cndmask_b32_e32 v248, v12, v11, vcc
	v_cndmask_b32_e64 v249, v12, v11, s[36:37]
	v_add_u32_e32 v248, 0xffffb000, v248
	v_add_u32_e32 v249, 0xffffa800, v249
	global_load_dwordx4 v[56:59], v248, s[8:9]
	v_lshrrev_b32_e32 v250, 1, v248
	global_load_dwordx2 v[104:105], v250, s[10:11]
	global_load_dwordx4 v[60:63], v249, s[8:9]
	v_lshrrev_b32_e32 v250, 1, v249
	global_load_dwordx2 v[106:107], v250, s[10:11]
	v_cmp_lt_u32_e32 vcc, 12, v6
	v_cmp_lt_u32_e64 s[36:37], 13, v6
	s_nop 0
	v_cndmask_b32_e32 v248, v12, v11, vcc
	v_cndmask_b32_e64 v249, v12, v11, s[36:37]
	v_add_u32_e32 v248, 0xffffa000, v248
	v_add_u32_e32 v249, 0xffff9800, v249
	global_load_dwordx4 v[64:67], v248, s[8:9]
	v_lshrrev_b32_e32 v250, 1, v248
	global_load_dwordx2 v[108:109], v250, s[10:11]
	global_load_dwordx4 v[68:71], v249, s[8:9]
	v_lshrrev_b32_e32 v250, 1, v249
	global_load_dwordx2 v[110:111], v250, s[10:11]
	v_cmp_lt_u32_e32 vcc, 14, v6
	v_cmp_lt_u32_e64 s[36:37], 15, v6
	s_nop 0
	v_cndmask_b32_e32 v248, v12, v11, vcc
	v_cndmask_b32_e64 v249, v12, v11, s[36:37]
	v_add_u32_e32 v248, 0xffff9000, v248
	v_add_u32_e32 v249, 0xffff8800, v249
	global_load_dwordx4 v[72:75], v248, s[8:9]
	v_lshrrev_b32_e32 v250, 1, v248
	global_load_dwordx2 v[112:113], v250, s[10:11]
	global_load_dwordx4 v[76:79], v249, s[8:9]
	v_lshrrev_b32_e32 v250, 1, v249
	global_load_dwordx2 v[114:115], v250, s[10:11]
	v_cmp_lt_u32_e32 vcc, 16, v6
	s_nop 1
	v_cndmask_b32_e32 v248, v12, v11, vcc
	v_add_u32_e32 v248, 0xffff8000, v248
	global_load_dwordx4 v[80:83], v248, s[8:9]
	v_lshrrev_b32_e32 v250, 1, v248
	global_load_dwordx2 v[116:117], v250, s[10:11]
	s_waitcnt vmcnt(32)
	v_lshlrev_b32_e32 v224, 16, v84
	v_and_b32_e32 v225, 0xffff0000, v84
	v_lshlrev_b32_e32 v226, 16, v85
	v_and_b32_e32 v227, 0xffff0000, v85
	v_mov_b32_e32 v220, v16
	v_mov_b32_e32 v221, v17
	v_mov_b32_e32 v222, v18
	v_mov_b32_e32 v223, v19
	s_waitcnt vmcnt(30)
	v_lshlrev_b32_e32 v248, 16, v86
	v_and_b32_e32 v249, 0xffff0000, v86
	v_lshlrev_b32_e32 v250, 16, v87
	v_and_b32_e32 v251, 0xffff0000, v87
	v_fma_f32 v224, v20, v224, v248
	v_fma_f32 v225, v21, v225, v249
	v_fma_f32 v226, v22, v226, v250
	v_fma_f32 v227, v23, v227, v251
	v_mul_f32_e32 v220, v220, v20
	v_mul_f32_e32 v221, v221, v21
	v_mul_f32_e32 v222, v222, v22
	v_mul_f32_e32 v223, v223, v23
	s_waitcnt vmcnt(28)
	v_lshlrev_b32_e32 v248, 16, v88
	v_and_b32_e32 v249, 0xffff0000, v88
	v_lshlrev_b32_e32 v250, 16, v89
	v_and_b32_e32 v251, 0xffff0000, v89
	v_fma_f32 v224, v24, v224, v248
	v_fma_f32 v225, v25, v225, v249
	v_fma_f32 v226, v26, v226, v250
	v_fma_f32 v227, v27, v227, v251
	v_mul_f32_e32 v220, v220, v24
	v_mul_f32_e32 v221, v221, v25
	v_mul_f32_e32 v222, v222, v26
	v_mul_f32_e32 v223, v223, v27
	s_waitcnt vmcnt(26)
	v_lshlrev_b32_e32 v248, 16, v90
	v_and_b32_e32 v249, 0xffff0000, v90
	v_lshlrev_b32_e32 v250, 16, v91
	v_and_b32_e32 v251, 0xffff0000, v91
	v_fma_f32 v224, v28, v224, v248
	v_fma_f32 v225, v29, v225, v249
	v_fma_f32 v226, v30, v226, v250
	v_fma_f32 v227, v31, v227, v251
	v_mul_f32_e32 v220, v220, v28
	v_mul_f32_e32 v221, v221, v29
	v_mul_f32_e32 v222, v222, v30
	v_mul_f32_e32 v223, v223, v31
	s_waitcnt vmcnt(24)
	v_lshlrev_b32_e32 v248, 16, v92
	v_and_b32_e32 v249, 0xffff0000, v92
	v_lshlrev_b32_e32 v250, 16, v93
	v_and_b32_e32 v251, 0xffff0000, v93
	v_fma_f32 v224, v32, v224, v248
	v_fma_f32 v225, v33, v225, v249
	v_fma_f32 v226, v34, v226, v250
	v_fma_f32 v227, v35, v227, v251
	v_mul_f32_e32 v220, v220, v32
	v_mul_f32_e32 v221, v221, v33
	v_mul_f32_e32 v222, v222, v34
	v_mul_f32_e32 v223, v223, v35
	s_waitcnt vmcnt(22)
	v_lshlrev_b32_e32 v248, 16, v94
	v_and_b32_e32 v249, 0xffff0000, v94
	v_lshlrev_b32_e32 v250, 16, v95
	v_and_b32_e32 v251, 0xffff0000, v95
	v_fma_f32 v224, v36, v224, v248
	v_fma_f32 v225, v37, v225, v249
	v_fma_f32 v226, v38, v226, v250
	v_fma_f32 v227, v39, v227, v251
	v_mul_f32_e32 v220, v220, v36
	v_mul_f32_e32 v221, v221, v37
	v_mul_f32_e32 v222, v222, v38
	v_mul_f32_e32 v223, v223, v39
	s_waitcnt vmcnt(20)
	v_lshlrev_b32_e32 v248, 16, v96
	v_and_b32_e32 v249, 0xffff0000, v96
	v_lshlrev_b32_e32 v250, 16, v97
	v_and_b32_e32 v251, 0xffff0000, v97
	v_fma_f32 v224, v40, v224, v248
	v_fma_f32 v225, v41, v225, v249
	v_fma_f32 v226, v42, v226, v250
	v_fma_f32 v227, v43, v227, v251
	v_mul_f32_e32 v220, v220, v40
	v_mul_f32_e32 v221, v221, v41
	v_mul_f32_e32 v222, v222, v42
	v_mul_f32_e32 v223, v223, v43
	s_waitcnt vmcnt(18)
	v_lshlrev_b32_e32 v248, 16, v98
	v_and_b32_e32 v249, 0xffff0000, v98
	v_lshlrev_b32_e32 v250, 16, v99
	v_and_b32_e32 v251, 0xffff0000, v99
	v_fma_f32 v224, v44, v224, v248
	v_fma_f32 v225, v45, v225, v249
	v_fma_f32 v226, v46, v226, v250
	v_fma_f32 v227, v47, v227, v251
	v_mul_f32_e32 v220, v220, v44
	v_mul_f32_e32 v221, v221, v45
	v_mul_f32_e32 v222, v222, v46
	v_mul_f32_e32 v223, v223, v47
	s_waitcnt vmcnt(16)
	v_lshlrev_b32_e32 v248, 16, v100
	v_and_b32_e32 v249, 0xffff0000, v100
	v_lshlrev_b32_e32 v250, 16, v101
	v_and_b32_e32 v251, 0xffff0000, v101
	v_fma_f32 v224, v48, v224, v248
	v_fma_f32 v225, v49, v225, v249
	v_fma_f32 v226, v50, v226, v250
	v_fma_f32 v227, v51, v227, v251
	v_mul_f32_e32 v220, v220, v48
	v_mul_f32_e32 v221, v221, v49
	v_mul_f32_e32 v222, v222, v50
	v_mul_f32_e32 v223, v223, v51
	s_waitcnt vmcnt(14)
	v_lshlrev_b32_e32 v248, 16, v102
	v_and_b32_e32 v249, 0xffff0000, v102
	v_lshlrev_b32_e32 v250, 16, v103
	v_and_b32_e32 v251, 0xffff0000, v103
	v_fma_f32 v224, v52, v224, v248
	v_fma_f32 v225, v53, v225, v249
	v_fma_f32 v226, v54, v226, v250
	v_fma_f32 v227, v55, v227, v251
	v_mul_f32_e32 v220, v220, v52
	v_mul_f32_e32 v221, v221, v53
	v_mul_f32_e32 v222, v222, v54
	v_mul_f32_e32 v223, v223, v55
	s_waitcnt vmcnt(12)
	v_lshlrev_b32_e32 v248, 16, v104
	v_and_b32_e32 v249, 0xffff0000, v104
	v_lshlrev_b32_e32 v250, 16, v105
	v_and_b32_e32 v251, 0xffff0000, v105
	v_fma_f32 v224, v56, v224, v248
	v_fma_f32 v225, v57, v225, v249
	v_fma_f32 v226, v58, v226, v250
	v_fma_f32 v227, v59, v227, v251
	v_mul_f32_e32 v220, v220, v56
	v_mul_f32_e32 v221, v221, v57
	v_mul_f32_e32 v222, v222, v58
	v_mul_f32_e32 v223, v223, v59
	s_waitcnt vmcnt(10)
	v_lshlrev_b32_e32 v248, 16, v106
	v_and_b32_e32 v249, 0xffff0000, v106
	v_lshlrev_b32_e32 v250, 16, v107
	v_and_b32_e32 v251, 0xffff0000, v107
	v_fma_f32 v224, v60, v224, v248
	v_fma_f32 v225, v61, v225, v249
	v_fma_f32 v226, v62, v226, v250
	v_fma_f32 v227, v63, v227, v251
	v_mul_f32_e32 v220, v220, v60
	v_mul_f32_e32 v221, v221, v61
	v_mul_f32_e32 v222, v222, v62
	v_mul_f32_e32 v223, v223, v63
	s_waitcnt vmcnt(8)
	v_lshlrev_b32_e32 v248, 16, v108
	v_and_b32_e32 v249, 0xffff0000, v108
	v_lshlrev_b32_e32 v250, 16, v109
	v_and_b32_e32 v251, 0xffff0000, v109
	v_fma_f32 v224, v64, v224, v248
	v_fma_f32 v225, v65, v225, v249
	v_fma_f32 v226, v66, v226, v250
	v_fma_f32 v227, v67, v227, v251
	v_mul_f32_e32 v220, v220, v64
	v_mul_f32_e32 v221, v221, v65
	v_mul_f32_e32 v222, v222, v66
	v_mul_f32_e32 v223, v223, v67
	s_waitcnt vmcnt(6)
	v_lshlrev_b32_e32 v248, 16, v110
	v_and_b32_e32 v249, 0xffff0000, v110
	v_lshlrev_b32_e32 v250, 16, v111
	v_and_b32_e32 v251, 0xffff0000, v111
	v_fma_f32 v224, v68, v224, v248
	v_fma_f32 v225, v69, v225, v249
	v_fma_f32 v226, v70, v226, v250
	v_fma_f32 v227, v71, v227, v251
	v_mul_f32_e32 v220, v220, v68
	v_mul_f32_e32 v221, v221, v69
	v_mul_f32_e32 v222, v222, v70
	v_mul_f32_e32 v223, v223, v71
	s_waitcnt vmcnt(4)
	v_lshlrev_b32_e32 v248, 16, v112
	v_and_b32_e32 v249, 0xffff0000, v112
	v_lshlrev_b32_e32 v250, 16, v113
	v_and_b32_e32 v251, 0xffff0000, v113
	v_fma_f32 v224, v72, v224, v248
	v_fma_f32 v225, v73, v225, v249
	v_fma_f32 v226, v74, v226, v250
	v_fma_f32 v227, v75, v227, v251
	v_mul_f32_e32 v220, v220, v72
	v_mul_f32_e32 v221, v221, v73
	v_mul_f32_e32 v222, v222, v74
	v_mul_f32_e32 v223, v223, v75
	s_waitcnt vmcnt(2)
	v_lshlrev_b32_e32 v248, 16, v114
	v_and_b32_e32 v249, 0xffff0000, v114
	v_lshlrev_b32_e32 v250, 16, v115
	v_and_b32_e32 v251, 0xffff0000, v115
	v_fma_f32 v224, v76, v224, v248
	v_fma_f32 v225, v77, v225, v249
	v_fma_f32 v226, v78, v226, v250
	v_fma_f32 v227, v79, v227, v251
	v_mul_f32_e32 v220, v220, v76
	v_mul_f32_e32 v221, v221, v77
	v_mul_f32_e32 v222, v222, v78
	v_mul_f32_e32 v223, v223, v79
	s_waitcnt vmcnt(0)
	v_lshlrev_b32_e32 v248, 16, v116
	v_and_b32_e32 v249, 0xffff0000, v116
	v_lshlrev_b32_e32 v250, 16, v117
	v_and_b32_e32 v251, 0xffff0000, v117
	v_fma_f32 v224, v80, v224, v248
	v_fma_f32 v225, v81, v225, v249
	v_fma_f32 v226, v82, v226, v250
	v_fma_f32 v227, v83, v227, v251
	v_mul_f32_e32 v220, v220, v80
	v_mul_f32_e32 v221, v221, v81
	v_mul_f32_e32 v222, v222, v82
	v_mul_f32_e32 v223, v223, v83
	v_cmp_le_u32_e32 vcc, 2, v1
	v_add_u32_e32 v252, 0xfffffff8, v7
	ds_bpermute_b32 v228, v252, v220
	ds_bpermute_b32 v229, v252, v221
	ds_bpermute_b32 v230, v252, v222
	ds_bpermute_b32 v231, v252, v223
	ds_bpermute_b32 v232, v252, v224
	ds_bpermute_b32 v233, v252, v225
	ds_bpermute_b32 v234, v252, v226
	ds_bpermute_b32 v235, v252, v227
	s_waitcnt lgkmcnt(0)
	v_fma_f32 v248, v220, v232, v224
	v_fma_f32 v249, v221, v233, v225
	v_fma_f32 v250, v222, v234, v226
	v_fma_f32 v251, v223, v235, v227
	v_mul_f32_e32 v228, v220, v228
	v_mul_f32_e32 v229, v221, v229
	v_mul_f32_e32 v230, v222, v230
	v_mul_f32_e32 v231, v223, v231
	v_cndmask_b32_e32 v224, v224, v248, vcc
	v_cndmask_b32_e32 v225, v225, v249, vcc
	v_cndmask_b32_e32 v226, v226, v250, vcc
	v_cndmask_b32_e32 v227, v227, v251, vcc
	v_cndmask_b32_e32 v220, v220, v228, vcc
	v_cndmask_b32_e32 v221, v221, v229, vcc
	v_cndmask_b32_e32 v222, v222, v230, vcc
	v_cndmask_b32_e32 v223, v223, v231, vcc
	v_cmp_le_u32_e32 vcc, 4, v1
	v_add_u32_e32 v252, 0xfffffff0, v7
	ds_bpermute_b32 v228, v252, v220
	ds_bpermute_b32 v229, v252, v221
	ds_bpermute_b32 v230, v252, v222
	ds_bpermute_b32 v231, v252, v223
	ds_bpermute_b32 v232, v252, v224
	ds_bpermute_b32 v233, v252, v225
	ds_bpermute_b32 v234, v252, v226
	ds_bpermute_b32 v235, v252, v227
	s_waitcnt lgkmcnt(0)
	v_fma_f32 v248, v220, v232, v224
	v_fma_f32 v249, v221, v233, v225
	v_fma_f32 v250, v222, v234, v226
	v_fma_f32 v251, v223, v235, v227
	v_mul_f32_e32 v228, v220, v228
	v_mul_f32_e32 v229, v221, v229
	v_mul_f32_e32 v230, v222, v230
	v_mul_f32_e32 v231, v223, v231
	v_cndmask_b32_e32 v224, v224, v248, vcc
	v_cndmask_b32_e32 v225, v225, v249, vcc
	v_cndmask_b32_e32 v226, v226, v250, vcc
	v_cndmask_b32_e32 v227, v227, v251, vcc
	v_cndmask_b32_e32 v220, v220, v228, vcc
	v_cndmask_b32_e32 v221, v221, v229, vcc
	v_cndmask_b32_e32 v222, v222, v230, vcc
	v_cndmask_b32_e32 v223, v223, v231, vcc
	v_cmp_le_u32_e32 vcc, 8, v1
	v_add_u32_e32 v252, 0xffffffe0, v7
	ds_bpermute_b32 v228, v252, v220
	ds_bpermute_b32 v229, v252, v221
	ds_bpermute_b32 v230, v252, v222
	ds_bpermute_b32 v231, v252, v223
	ds_bpermute_b32 v232, v252, v224
	ds_bpermute_b32 v233, v252, v225
	ds_bpermute_b32 v234, v252, v226
	ds_bpermute_b32 v235, v252, v227
	s_waitcnt lgkmcnt(0)
	v_fma_f32 v248, v220, v232, v224
	v_fma_f32 v249, v221, v233, v225
	v_fma_f32 v250, v222, v234, v226
	v_fma_f32 v251, v223, v235, v227
	v_mul_f32_e32 v228, v220, v228
	v_mul_f32_e32 v229, v221, v229
	v_mul_f32_e32 v230, v222, v230
	v_mul_f32_e32 v231, v223, v231
	v_cndmask_b32_e32 v224, v224, v248, vcc
	v_cndmask_b32_e32 v225, v225, v249, vcc
	v_cndmask_b32_e32 v226, v226, v250, vcc
	v_cndmask_b32_e32 v227, v227, v251, vcc
	v_cndmask_b32_e32 v220, v220, v228, vcc
	v_cndmask_b32_e32 v221, v221, v229, vcc
	v_cndmask_b32_e32 v222, v222, v230, vcc
	v_cndmask_b32_e32 v223, v223, v231, vcc
	v_cmp_le_u32_e32 vcc, 16, v1
	v_add_u32_e32 v252, 0xffffffc0, v7
	ds_bpermute_b32 v228, v252, v220
	ds_bpermute_b32 v229, v252, v221
	ds_bpermute_b32 v230, v252, v222
	ds_bpermute_b32 v231, v252, v223
	ds_bpermute_b32 v232, v252, v224
	ds_bpermute_b32 v233, v252, v225
	ds_bpermute_b32 v234, v252, v226
	ds_bpermute_b32 v235, v252, v227
	s_waitcnt lgkmcnt(0)
	v_fma_f32 v248, v220, v232, v224
	v_fma_f32 v249, v221, v233, v225
	v_fma_f32 v250, v222, v234, v226
	v_fma_f32 v251, v223, v235, v227
	v_mul_f32_e32 v228, v220, v228
	v_mul_f32_e32 v229, v221, v229
	v_mul_f32_e32 v230, v222, v230
	v_mul_f32_e32 v231, v223, v231
	v_cndmask_b32_e32 v224, v224, v248, vcc
	v_cndmask_b32_e32 v225, v225, v249, vcc
	v_cndmask_b32_e32 v226, v226, v250, vcc
	v_cndmask_b32_e32 v227, v227, v251, vcc
	v_cndmask_b32_e32 v220, v220, v228, vcc
	v_cndmask_b32_e32 v221, v221, v229, vcc
	v_cndmask_b32_e32 v222, v222, v230, vcc
	v_cndmask_b32_e32 v223, v223, v231, vcc
	v_cmp_le_u32_e32 vcc, 32, v1
	v_add_u32_e32 v252, 0xffffff80, v7
	ds_bpermute_b32 v228, v252, v220
	ds_bpermute_b32 v229, v252, v221
	ds_bpermute_b32 v230, v252, v222
	ds_bpermute_b32 v231, v252, v223
	ds_bpermute_b32 v232, v252, v224
	ds_bpermute_b32 v233, v252, v225
	ds_bpermute_b32 v234, v252, v226
	ds_bpermute_b32 v235, v252, v227
	s_waitcnt lgkmcnt(0)
	v_fma_f32 v248, v220, v232, v224
	v_fma_f32 v249, v221, v233, v225
	v_fma_f32 v250, v222, v234, v226
	v_fma_f32 v251, v223, v235, v227
	v_mul_f32_e32 v228, v220, v228
	v_mul_f32_e32 v229, v221, v229
	v_mul_f32_e32 v230, v222, v230
	v_mul_f32_e32 v231, v223, v231
	v_cndmask_b32_e32 v224, v224, v248, vcc
	v_cndmask_b32_e32 v225, v225, v249, vcc
	v_cndmask_b32_e32 v226, v226, v250, vcc
	v_cndmask_b32_e32 v227, v227, v251, vcc
	v_cndmask_b32_e32 v220, v220, v228, vcc
	v_cndmask_b32_e32 v221, v221, v229, vcc
	v_cndmask_b32_e32 v222, v222, v230, vcc
	v_cndmask_b32_e32 v223, v223, v231, vcc
	v_cmp_lt_u32_e32 vcc, 61, v1
	s_lshl_b32 s13, s12, 6
	v_add_u32_e32 v252, s13, v8
	s_and_saveexec_b64 s[38:39], vcc
	ds_write_b128 v252, v[220:223]
	ds_write_b128 v252, v[224:227] offset:16
	s_or_b64 exec, exec, s[38:39]
	s_waitcnt lgkmcnt(0)
	s_barrier
	v_mov_b32_e32 v244, 0
	v_mov_b32_e32 v245, 0
	v_mov_b32_e32 v246, 0
	v_mov_b32_e32 v247, 0
	ds_read_b128 v[228:231], v8 offset:0
	ds_read_b128 v[232:235], v8 offset:16
	ds_read_b128 v[236:239], v8 offset:64
	ds_read_b128 v[240:243], v8 offset:80
	s_cmp_le_u32 s12, 0
	s_cbranch_scc1 .Lrg_cdone0
	s_waitcnt lgkmcnt(2)
	v_fma_f32 v244, v228, v244, v232
	v_fma_f32 v245, v229, v245, v233
	v_fma_f32 v246, v230, v246, v234
	v_fma_f32 v247, v231, v247, v235
	ds_read_b128 v[228:231], v8 offset:128
	ds_read_b128 v[232:235], v8 offset:144
	s_cmp_le_u32 s12, 1
	s_cbranch_scc1 .Lrg_cdone0
	s_waitcnt lgkmcnt(2)
	v_fma_f32 v244, v236, v244, v240
	v_fma_f32 v245, v237, v245, v241
	v_fma_f32 v246, v238, v246, v242
	v_fma_f32 v247, v239, v247, v243
	ds_read_b128 v[236:239], v8 offset:192
	ds_read_b128 v[240:243], v8 offset:208
	s_cmp_le_u32 s12, 2
	s_cbranch_scc1 .Lrg_cdone0
	s_waitcnt lgkmcnt(2)
	v_fma_f32 v244, v228, v244, v232
	v_fma_f32 v245, v229, v245, v233
	v_fma_f32 v246, v230, v246, v234
	v_fma_f32 v247, v231, v247, v235
	ds_read_b128 v[228:231], v8 offset:256
	ds_read_b128 v[232:235], v8 offset:272
	s_cmp_le_u32 s12, 3
	s_cbranch_scc1 .Lrg_cdone0
	s_waitcnt lgkmcnt(2)
	v_fma_f32 v244, v236, v244, v240
	v_fma_f32 v245, v237, v245, v241
	v_fma_f32 v246, v238, v246, v242
	v_fma_f32 v247, v239, v247, v243
	ds_read_b128 v[236:239], v8 offset:320
	ds_read_b128 v[240:243], v8 offset:336
	s_cmp_le_u32 s12, 4
	s_cbranch_scc1 .Lrg_cdone0
	s_waitcnt lgkmcnt(2)
	v_fma_f32 v244, v228, v244, v232
	v_fma_f32 v245, v229, v245, v233
	v_fma_f32 v246, v230, v246, v234
	v_fma_f32 v247, v231, v247, v235
	ds_read_b128 v[228:231], v8 offset:384
	ds_read_b128 v[232:235], v8 offset:400
	s_cmp_le_u32 s12, 5
	s_cbranch_scc1 .Lrg_cdone0
	s_waitcnt lgkmcnt(2)
	v_fma_f32 v244, v236, v244, v240
	v_fma_f32 v245, v237, v245, v241
	v_fma_f32 v246, v238, v246, v242
	v_fma_f32 v247, v239, v247, v243
	s_cmp_le_u32 s12, 6
	s_cbranch_scc1 .Lrg_cdone0
	s_waitcnt lgkmcnt(0)
	v_fma_f32 v244, v228, v244, v232
	v_fma_f32 v245, v229, v245, v233
	v_fma_f32 v246, v230, v246, v234
	v_fma_f32 v247, v231, v247, v235
.Lrg_cdone0:
	s_waitcnt lgkmcnt(0)
	v_cmp_le_u32_e32 vcc, 2, v1
	v_add_u32_e32 v252, -8, v7
	ds_bpermute_b32 v228, v252, v220
	ds_bpermute_b32 v229, v252, v221
	ds_bpermute_b32 v230, v252, v222
	ds_bpermute_b32 v231, v252, v223
	ds_bpermute_b32 v232, v252, v224
	ds_bpermute_b32 v233, v252, v225
	ds_bpermute_b32 v234, v252, v226
	ds_bpermute_b32 v235, v252, v227
	s_waitcnt lgkmcnt(0)
	v_fma_f32 v248, v228, v244, v232
	v_fma_f32 v249, v229, v245, v233
	v_fma_f32 v250, v230, v246, v234
	v_fma_f32 v251, v231, v247, v235
	v_cndmask_b32_e32 v244, v244, v248, vcc
	v_cndmask_b32_e32 v245, v245, v249, vcc
	v_cndmask_b32_e32 v246, v246, v250, vcc
	v_cndmask_b32_e32 v247, v247, v251, vcc
	v_lshlrev_b32_e32 v248, 16, v84
	v_and_b32_e32 v249, 0xffff0000, v84
	v_lshlrev_b32_e32 v250, 16, v85
	v_and_b32_e32 v251, 0xffff0000, v85
	v_fma_f32 v16, v16, v244, v248
	v_fma_f32 v17, v17, v245, v249
	v_fma_f32 v18, v18, v246, v250
	v_fma_f32 v19, v19, v247, v251
	v_cmp_lt_u32_e32 vcc, 0, v6
	s_nop 1
	v_cndmask_b32_e32 v252, v12, v11, vcc
	global_store_dwordx4 v252, v[16:19], s[58:59]
	v_lshlrev_b32_e32 v248, 16, v86
	v_and_b32_e32 v249, 0xffff0000, v86
	v_lshlrev_b32_e32 v250, 16, v87
	v_and_b32_e32 v251, 0xffff0000, v87
	v_fma_f32 v20, v20, v16, v248
	v_fma_f32 v21, v21, v17, v249
	v_fma_f32 v22, v22, v18, v250
	v_fma_f32 v23, v23, v19, v251
	v_cmp_lt_u32_e32 vcc, 1, v6
	s_nop 1
	v_cndmask_b32_e32 v252, v12, v11, vcc
	v_add_u32_e32 v252, 0xfffff800, v252
	global_store_dwordx4 v252, v[20:23], s[58:59]
	v_lshlrev_b32_e32 v248, 16, v88
	v_and_b32_e32 v249, 0xffff0000, v88
	v_lshlrev_b32_e32 v250, 16, v89
	v_and_b32_e32 v251, 0xffff0000, v89
	v_fma_f32 v24, v24, v20, v248
	v_fma_f32 v25, v25, v21, v249
	v_fma_f32 v26, v26, v22, v250
	v_fma_f32 v27, v27, v23, v251
	v_cmp_lt_u32_e32 vcc, 2, v6
	s_nop 1
	v_cndmask_b32_e32 v252, v12, v11, vcc
	v_add_u32_e32 v252, 0xfffff000, v252
	global_store_dwordx4 v252, v[24:27], s[58:59]
	v_lshlrev_b32_e32 v248, 16, v90
	v_and_b32_e32 v249, 0xffff0000, v90
	v_lshlrev_b32_e32 v250, 16, v91
	v_and_b32_e32 v251, 0xffff0000, v91
	v_fma_f32 v28, v28, v24, v248
	v_fma_f32 v29, v29, v25, v249
	v_fma_f32 v30, v30, v26, v250
	v_fma_f32 v31, v31, v27, v251
	v_cmp_lt_u32_e32 vcc, 3, v6
	s_nop 1
	v_cndmask_b32_e32 v252, v12, v11, vcc
	v_add_u32_e32 v252, 0xffffe800, v252
	global_store_dwordx4 v252, v[28:31], s[58:59]
	v_lshlrev_b32_e32 v248, 16, v92
	v_and_b32_e32 v249, 0xffff0000, v92
	v_lshlrev_b32_e32 v250, 16, v93
	v_and_b32_e32 v251, 0xffff0000, v93
	v_fma_f32 v32, v32, v28, v248
	v_fma_f32 v33, v33, v29, v249
	v_fma_f32 v34, v34, v30, v250
	v_fma_f32 v35, v35, v31, v251
	v_cmp_lt_u32_e32 vcc, 4, v6
	s_nop 1
	v_cndmask_b32_e32 v252, v12, v11, vcc
	v_add_u32_e32 v252, 0xffffe000, v252
	global_store_dwordx4 v252, v[32:35], s[58:59]
	v_lshlrev_b32_e32 v248, 16, v94
	v_and_b32_e32 v249, 0xffff0000, v94
	v_lshlrev_b32_e32 v250, 16, v95
	v_and_b32_e32 v251, 0xffff0000, v95
	v_fma_f32 v36, v36, v32, v248
	v_fma_f32 v37, v37, v33, v249
	v_fma_f32 v38, v38, v34, v250
	v_fma_f32 v39, v39, v35, v251
	v_cmp_lt_u32_e32 vcc, 5, v6
	s_nop 1
	v_cndmask_b32_e32 v252, v12, v11, vcc
	v_add_u32_e32 v252, 0xffffd800, v252
	global_store_dwordx4 v252, v[36:39], s[58:59]
	v_lshlrev_b32_e32 v248, 16, v96
	v_and_b32_e32 v249, 0xffff0000, v96
	v_lshlrev_b32_e32 v250, 16, v97
	v_and_b32_e32 v251, 0xffff0000, v97
	v_fma_f32 v40, v40, v36, v248
	v_fma_f32 v41, v41, v37, v249
	v_fma_f32 v42, v42, v38, v250
	v_fma_f32 v43, v43, v39, v251
	v_cmp_lt_u32_e32 vcc, 6, v6
	s_nop 1
	v_cndmask_b32_e32 v252, v12, v11, vcc
	v_add_u32_e32 v252, 0xffffd000, v252
	global_store_dwordx4 v252, v[40:43], s[58:59]
	v_lshlrev_b32_e32 v248, 16, v98
	v_and_b32_e32 v249, 0xffff0000, v98
	v_lshlrev_b32_e32 v250, 16, v99
	v_and_b32_e32 v251, 0xffff0000, v99
	v_fma_f32 v44, v44, v40, v248
	v_fma_f32 v45, v45, v41, v249
	v_fma_f32 v46, v46, v42, v250
	v_fma_f32 v47, v47, v43, v251
	v_cmp_lt_u32_e32 vcc, 7, v6
	s_nop 1
	v_cndmask_b32_e32 v252, v12, v11, vcc
	v_add_u32_e32 v252, 0xffffc800, v252
	global_store_dwordx4 v252, v[44:47], s[58:59]
	v_lshlrev_b32_e32 v248, 16, v100
	v_and_b32_e32 v249, 0xffff0000, v100
	v_lshlrev_b32_e32 v250, 16, v101
	v_and_b32_e32 v251, 0xffff0000, v101
	v_fma_f32 v48, v48, v44, v248
	v_fma_f32 v49, v49, v45, v249
	v_fma_f32 v50, v50, v46, v250
	v_fma_f32 v51, v51, v47, v251
	v_cmp_lt_u32_e32 vcc, 8, v6
	s_nop 1
	v_cndmask_b32_e32 v252, v12, v11, vcc
	v_add_u32_e32 v252, 0xffffc000, v252
	global_store_dwordx4 v252, v[48:51], s[58:59]
	v_lshlrev_b32_e32 v248, 16, v102
	v_and_b32_e32 v249, 0xffff0000, v102
	v_lshlrev_b32_e32 v250, 16, v103
	v_and_b32_e32 v251, 0xffff0000, v103
	v_fma_f32 v52, v52, v48, v248
	v_fma_f32 v53, v53, v49, v249
	v_fma_f32 v54, v54, v50, v250
	v_fma_f32 v55, v55, v51, v251
	v_cmp_lt_u32_e32 vcc, 9, v6
	s_nop 1
	v_cndmask_b32_e32 v252, v12, v11, vcc
	v_add_u32_e32 v252, 0xffffb800, v252
	global_store_dwordx4 v252, v[52:55], s[58:59]
	v_lshlrev_b32_e32 v248, 16, v104
	v_and_b32_e32 v249, 0xffff0000, v104
	v_lshlrev_b32_e32 v250, 16, v105
	v_and_b32_e32 v251, 0xffff0000, v105
	v_fma_f32 v56, v56, v52, v248
	v_fma_f32 v57, v57, v53, v249
	v_fma_f32 v58, v58, v54, v250
	v_fma_f32 v59, v59, v55, v251
	v_cmp_lt_u32_e32 vcc, 10, v6
	s_nop 1
	v_cndmask_b32_e32 v252, v12, v11, vcc
	v_add_u32_e32 v252, 0xffffb000, v252
	global_store_dwordx4 v252, v[56:59], s[58:59]
	v_lshlrev_b32_e32 v248, 16, v106
	v_and_b32_e32 v249, 0xffff0000, v106
	v_lshlrev_b32_e32 v250, 16, v107
	v_and_b32_e32 v251, 0xffff0000, v107
	v_fma_f32 v60, v60, v56, v248
	v_fma_f32 v61, v61, v57, v249
	v_fma_f32 v62, v62, v58, v250
	v_fma_f32 v63, v63, v59, v251
	v_cmp_lt_u32_e32 vcc, 11, v6
	s_nop 1
	v_cndmask_b32_e32 v252, v12, v11, vcc
	v_add_u32_e32 v252, 0xffffa800, v252
	global_store_dwordx4 v252, v[60:63], s[58:59]
	v_lshlrev_b32_e32 v248, 16, v108
	v_and_b32_e32 v249, 0xffff0000, v108
	v_lshlrev_b32_e32 v250, 16, v109
	v_and_b32_e32 v251, 0xffff0000, v109
	v_fma_f32 v64, v64, v60, v248
	v_fma_f32 v65, v65, v61, v249
	v_fma_f32 v66, v66, v62, v250
	v_fma_f32 v67, v67, v63, v251
	v_cmp_lt_u32_e32 vcc, 12, v6
	s_nop 1
	v_cndmask_b32_e32 v252, v12, v11, vcc
	v_add_u32_e32 v252, 0xffffa000, v252
	global_store_dwordx4 v252, v[64:67], s[58:59]
	v_lshlrev_b32_e32 v248, 16, v110
	v_and_b32_e32 v249, 0xffff0000, v110
	v_lshlrev_b32_e32 v250, 16, v111
	v_and_b32_e32 v251, 0xffff0000, v111
	v_fma_f32 v68, v68, v64, v248
	v_fma_f32 v69, v69, v65, v249
	v_fma_f32 v70, v70, v66, v250
	v_fma_f32 v71, v71, v67, v251
	v_cmp_lt_u32_e32 vcc, 13, v6
	s_nop 1
	v_cndmask_b32_e32 v252, v12, v11, vcc
	v_add_u32_e32 v252, 0xffff9800, v252
	global_store_dwordx4 v252, v[68:71], s[58:59]
	v_lshlrev_b32_e32 v248, 16, v112
	v_and_b32_e32 v249, 0xffff0000, v112
	v_lshlrev_b32_e32 v250, 16, v113
	v_and_b32_e32 v251, 0xffff0000, v113
	v_fma_f32 v72, v72, v68, v248
	v_fma_f32 v73, v73, v69, v249
	v_fma_f32 v74, v74, v70, v250
	v_fma_f32 v75, v75, v71, v251
	v_cmp_lt_u32_e32 vcc, 14, v6
	s_nop 1
	v_cndmask_b32_e32 v252, v12, v11, vcc
	v_add_u32_e32 v252, 0xffff9000, v252
	global_store_dwordx4 v252, v[72:75], s[58:59]
	v_lshlrev_b32_e32 v248, 16, v114
	v_and_b32_e32 v249, 0xffff0000, v114
	v_lshlrev_b32_e32 v250, 16, v115
	v_and_b32_e32 v251, 0xffff0000, v115
	v_fma_f32 v76, v76, v72, v248
	v_fma_f32 v77, v77, v73, v249
	v_fma_f32 v78, v78, v74, v250
	v_fma_f32 v79, v79, v75, v251
	v_cmp_lt_u32_e32 vcc, 15, v6
	s_nop 1
	v_cndmask_b32_e32 v252, v12, v11, vcc
	v_add_u32_e32 v252, 0xffff8800, v252
	global_store_dwordx4 v252, v[76:79], s[58:59]
	v_lshlrev_b32_e32 v248, 16, v116
	v_and_b32_e32 v249, 0xffff0000, v116
	v_lshlrev_b32_e32 v250, 16, v117
	v_and_b32_e32 v251, 0xffff0000, v117
	v_fma_f32 v80, v80, v76, v248
	v_fma_f32 v81, v81, v77, v249
	v_fma_f32 v82, v82, v78, v250
	v_fma_f32 v83, v83, v79, v251
	v_cmp_lt_u32_e32 vcc, 16, v6
	s_nop 1
	v_cndmask_b32_e32 v252, v12, v11, vcc
	v_add_u32_e32 v252, 0xffff8000, v252
	global_store_dwordx4 v252, v[80:83], s[58:59]
	s_waitcnt vmcnt(0)
	s_barrier
	s_add_u32 s8, s18, 0x0
	s_addc_u32 s9, s19, 0
	s_add_u32 s10, s20, 0x0
	s_addc_u32 s11, s21, 0
	s_add_i32 s13, s26, 0xffffff00
	v_add_u32_e32 v9, s27, v4
	v_add_u32_e32 v10, s13, v4
	v_lshl_add_u32 v11, v9, 11, v5
	v_lshl_add_u32 v12, v10, 11, v5
	v_lshrrev_b32_e32 v252, 1, v5
	v_add_u32_e32 v252, 0x1000, v252
	v_mad_u32_u24 v13, v9, s14, v252
	v_mad_u32_u24 v14, v10, s14, v252
	v_cmp_lt_u32_e32 vcc, 0, v6
	v_cmp_lt_u32_e64 s[36:37], 1, v6
	s_nop 0
	v_cndmask_b32_e32 v248, v12, v11, vcc
	v_cndmask_b32_e64 v249, v12, v11, s[36:37]
	v_add_u32_e32 v249, 0x800, v249
	global_load_dwordx4 v[16:19], v248, s[8:9]
	v_lshrrev_b32_e32 v250, 1, v248
	global_load_dwordx2 v[84:85], v250, s[10:11]
	global_load_dwordx4 v[20:23], v249, s[8:9]
	v_lshrrev_b32_e32 v250, 1, v249
	global_load_dwordx2 v[86:87], v250, s[10:11]
	v_cmp_lt_u32_e32 vcc, 2, v6
	v_cmp_lt_u32_e64 s[36:37], 3, v6
	s_nop 0
	v_cndmask_b32_e32 v248, v12, v11, vcc
	v_cndmask_b32_e64 v249, v12, v11, s[36:37]
	v_add_u32_e32 v248, 0x1000, v248
	v_add_u32_e32 v249, 0x1800, v249
	global_load_dwordx4 v[24:27], v248, s[8:9]
	v_lshrrev_b32_e32 v250, 1, v248
	global_load_dwordx2 v[88:89], v250, s[10:11]
	global_load_dwordx4 v[28:31], v249, s[8:9]
	v_lshrrev_b32_e32 v250, 1, v249
	global_load_dwordx2 v[90:91], v250, s[10:11]
	v_cmp_lt_u32_e32 vcc, 4, v6
	v_cmp_lt_u32_e64 s[36:37], 5, v6
	s_nop 0
	v_cndmask_b32_e32 v248, v12, v11, vcc
	v_cndmask_b32_e64 v249, v12, v11, s[36:37]
	v_add_u32_e32 v248, 0x2000, v248
	v_add_u32_e32 v249, 0x2800, v249
	global_load_dwordx4 v[32:35], v248, s[8:9]
	v_lshrrev_b32_e32 v250, 1, v248
	global_load_dwordx2 v[92:93], v250, s[10:11]
	global_load_dwordx4 v[36:39], v249, s[8:9]
	v_lshrrev_b32_e32 v250, 1, v249
	global_load_dwordx2 v[94:95], v250, s[10:11]
	v_cmp_lt_u32_e32 vcc, 6, v6
	v_cmp_lt_u32_e64 s[36:37], 7, v6
	s_nop 0
	v_cndmask_b32_e32 v248, v12, v11, vcc
	v_cndmask_b32_e64 v249, v12, v11, s[36:37]
	v_add_u32_e32 v248, 0x3000, v248
	v_add_u32_e32 v249, 0x3800, v249
	global_load_dwordx4 v[40:43], v248, s[8:9]
	v_lshrrev_b32_e32 v250, 1, v248
	global_load_dwordx2 v[96:97], v250, s[10:11]
	global_load_dwordx4 v[44:47], v249, s[8:9]
	v_lshrrev_b32_e32 v250, 1, v249
	global_load_dwordx2 v[98:99], v250, s[10:11]
	v_cmp_lt_u32_e32 vcc, 8, v6
	v_cmp_lt_u32_e64 s[36:37], 9, v6
	s_nop 0
	v_cndmask_b32_e32 v248, v12, v11, vcc
	v_cndmask_b32_e64 v249, v12, v11, s[36:37]
	v_add_u32_e32 v248, 0x4000, v248
	v_add_u32_e32 v249, 0x4800, v249
	global_load_dwordx4 v[48:51], v248, s[8:9]
	v_lshrrev_b32_e32 v250, 1, v248
	global_load_dwordx2 v[100:101], v250, s[10:11]
	global_load_dwordx4 v[52:55], v249, s[8:9]
	v_lshrrev_b32_e32 v250, 1, v249
	global_load_dwordx2 v[102:103], v250, s[10:11]
	v_cmp_lt_u32_e32 vcc, 10, v6
	v_cmp_lt_u32_e64 s[36:37], 11, v6
	s_nop 0
	v_cndmask_b32_e32 v248, v12, v11, vcc
	v_cndmask_b32_e64 v249, v12, v11, s[36:37]
	v_add_u32_e32 v248, 0x5000, v248
	v_add_u32_e32 v249, 0x5800, v249
	global_load_dwordx4 v[56:59], v248, s[8:9]
	v_lshrrev_b32_e32 v250, 1, v248
	global_load_dwordx2 v[104:105], v250, s[10:11]
	global_load_dwordx4 v[60:63], v249, s[8:9]
	v_lshrrev_b32_e32 v250, 1, v249
	global_load_dwordx2 v[106:107], v250, s[10:11]
	v_cmp_lt_u32_e32 vcc, 12, v6
	v_cmp_lt_u32_e64 s[36:37], 13, v6
	s_nop 0
	v_cndmask_b32_e32 v248, v12, v11, vcc
	v_cndmask_b32_e64 v249, v12, v11, s[36:37]
	v_add_u32_e32 v248, 0x6000, v248
	v_add_u32_e32 v249, 0x6800, v249
	global_load_dwordx4 v[64:67], v248, s[8:9]
	v_lshrrev_b32_e32 v250, 1, v248
	global_load_dwordx2 v[108:109], v250, s[10:11]
	global_load_dwordx4 v[68:71], v249, s[8:9]
	v_lshrrev_b32_e32 v250, 1, v249
	global_load_dwordx2 v[110:111], v250, s[10:11]
	v_cmp_lt_u32_e32 vcc, 14, v6
	v_cmp_lt_u32_e64 s[36:37], 15, v6
	s_nop 0
	v_cndmask_b32_e32 v248, v12, v11, vcc
	v_cndmask_b32_e64 v249, v12, v11, s[36:37]
	v_add_u32_e32 v248, 0x7000, v248
	v_add_u32_e32 v249, 0x7800, v249
	global_load_dwordx4 v[72:75], v248, s[8:9]
	v_lshrrev_b32_e32 v250, 1, v248
	global_load_dwordx2 v[112:113], v250, s[10:11]
	global_load_dwordx4 v[76:79], v249, s[8:9]
	v_lshrrev_b32_e32 v250, 1, v249
	global_load_dwordx2 v[114:115], v250, s[10:11]
	v_cmp_lt_u32_e32 vcc, 16, v6
	s_nop 1
	v_cndmask_b32_e32 v248, v12, v11, vcc
	v_add_u32_e32 v248, 0x8000, v248
	global_load_dwordx4 v[80:83], v248, s[8:9]
	v_lshrrev_b32_e32 v250, 1, v248
	global_load_dwordx2 v[116:117], v250, s[10:11]
	s_waitcnt vmcnt(32)
	v_lshlrev_b32_e32 v224, 16, v84
	v_and_b32_e32 v225, 0xffff0000, v84
	v_lshlrev_b32_e32 v226, 16, v85
	v_and_b32_e32 v227, 0xffff0000, v85
	v_mov_b32_e32 v220, v16
	v_mov_b32_e32 v221, v17
	v_mov_b32_e32 v222, v18
	v_mov_b32_e32 v223, v19
	s_waitcnt vmcnt(30)
	v_lshlrev_b32_e32 v248, 16, v86
	v_and_b32_e32 v249, 0xffff0000, v86
	v_lshlrev_b32_e32 v250, 16, v87
	v_and_b32_e32 v251, 0xffff0000, v87
	v_fma_f32 v224, v20, v224, v248
	v_fma_f32 v225, v21, v225, v249
	v_fma_f32 v226, v22, v226, v250
	v_fma_f32 v227, v23, v227, v251
	v_mul_f32_e32 v220, v220, v20
	v_mul_f32_e32 v221, v221, v21
	v_mul_f32_e32 v222, v222, v22
	v_mul_f32_e32 v223, v223, v23
	s_waitcnt vmcnt(28)
	v_lshlrev_b32_e32 v248, 16, v88
	v_and_b32_e32 v249, 0xffff0000, v88
	v_lshlrev_b32_e32 v250, 16, v89
	v_and_b32_e32 v251, 0xffff0000, v89
	v_fma_f32 v224, v24, v224, v248
	v_fma_f32 v225, v25, v225, v249
	v_fma_f32 v226, v26, v226, v250
	v_fma_f32 v227, v27, v227, v251
	v_mul_f32_e32 v220, v220, v24
	v_mul_f32_e32 v221, v221, v25
	v_mul_f32_e32 v222, v222, v26
	v_mul_f32_e32 v223, v223, v27
	s_waitcnt vmcnt(26)
	v_lshlrev_b32_e32 v248, 16, v90
	v_and_b32_e32 v249, 0xffff0000, v90
	v_lshlrev_b32_e32 v250, 16, v91
	v_and_b32_e32 v251, 0xffff0000, v91
	v_fma_f32 v224, v28, v224, v248
	v_fma_f32 v225, v29, v225, v249
	v_fma_f32 v226, v30, v226, v250
	v_fma_f32 v227, v31, v227, v251
	v_mul_f32_e32 v220, v220, v28
	v_mul_f32_e32 v221, v221, v29
	v_mul_f32_e32 v222, v222, v30
	v_mul_f32_e32 v223, v223, v31
	s_waitcnt vmcnt(24)
	v_lshlrev_b32_e32 v248, 16, v92
	v_and_b32_e32 v249, 0xffff0000, v92
	v_lshlrev_b32_e32 v250, 16, v93
	v_and_b32_e32 v251, 0xffff0000, v93
	v_fma_f32 v224, v32, v224, v248
	v_fma_f32 v225, v33, v225, v249
	v_fma_f32 v226, v34, v226, v250
	v_fma_f32 v227, v35, v227, v251
	v_mul_f32_e32 v220, v220, v32
	v_mul_f32_e32 v221, v221, v33
	v_mul_f32_e32 v222, v222, v34
	v_mul_f32_e32 v223, v223, v35
	s_waitcnt vmcnt(22)
	v_lshlrev_b32_e32 v248, 16, v94
	v_and_b32_e32 v249, 0xffff0000, v94
	v_lshlrev_b32_e32 v250, 16, v95
	v_and_b32_e32 v251, 0xffff0000, v95
	v_fma_f32 v224, v36, v224, v248
	v_fma_f32 v225, v37, v225, v249
	v_fma_f32 v226, v38, v226, v250
	v_fma_f32 v227, v39, v227, v251
	v_mul_f32_e32 v220, v220, v36
	v_mul_f32_e32 v221, v221, v37
	v_mul_f32_e32 v222, v222, v38
	v_mul_f32_e32 v223, v223, v39
	s_waitcnt vmcnt(20)
	v_lshlrev_b32_e32 v248, 16, v96
	v_and_b32_e32 v249, 0xffff0000, v96
	v_lshlrev_b32_e32 v250, 16, v97
	v_and_b32_e32 v251, 0xffff0000, v97
	v_fma_f32 v224, v40, v224, v248
	v_fma_f32 v225, v41, v225, v249
	v_fma_f32 v226, v42, v226, v250
	v_fma_f32 v227, v43, v227, v251
	v_mul_f32_e32 v220, v220, v40
	v_mul_f32_e32 v221, v221, v41
	v_mul_f32_e32 v222, v222, v42
	v_mul_f32_e32 v223, v223, v43
	s_waitcnt vmcnt(18)
	v_lshlrev_b32_e32 v248, 16, v98
	v_and_b32_e32 v249, 0xffff0000, v98
	v_lshlrev_b32_e32 v250, 16, v99
	v_and_b32_e32 v251, 0xffff0000, v99
	v_fma_f32 v224, v44, v224, v248
	v_fma_f32 v225, v45, v225, v249
	v_fma_f32 v226, v46, v226, v250
	v_fma_f32 v227, v47, v227, v251
	v_mul_f32_e32 v220, v220, v44
	v_mul_f32_e32 v221, v221, v45
	v_mul_f32_e32 v222, v222, v46
	v_mul_f32_e32 v223, v223, v47
	s_waitcnt vmcnt(16)
	v_lshlrev_b32_e32 v248, 16, v100
	v_and_b32_e32 v249, 0xffff0000, v100
	v_lshlrev_b32_e32 v250, 16, v101
	v_and_b32_e32 v251, 0xffff0000, v101
	v_fma_f32 v224, v48, v224, v248
	v_fma_f32 v225, v49, v225, v249
	v_fma_f32 v226, v50, v226, v250
	v_fma_f32 v227, v51, v227, v251
	v_mul_f32_e32 v220, v220, v48
	v_mul_f32_e32 v221, v221, v49
	v_mul_f32_e32 v222, v222, v50
	v_mul_f32_e32 v223, v223, v51
	s_waitcnt vmcnt(14)
	v_lshlrev_b32_e32 v248, 16, v102
	v_and_b32_e32 v249, 0xffff0000, v102
	v_lshlrev_b32_e32 v250, 16, v103
	v_and_b32_e32 v251, 0xffff0000, v103
	v_fma_f32 v224, v52, v224, v248
	v_fma_f32 v225, v53, v225, v249
	v_fma_f32 v226, v54, v226, v250
	v_fma_f32 v227, v55, v227, v251
	v_mul_f32_e32 v220, v220, v52
	v_mul_f32_e32 v221, v221, v53
	v_mul_f32_e32 v222, v222, v54
	v_mul_f32_e32 v223, v223, v55
	s_waitcnt vmcnt(12)
	v_lshlrev_b32_e32 v248, 16, v104
	v_and_b32_e32 v249, 0xffff0000, v104
	v_lshlrev_b32_e32 v250, 16, v105
	v_and_b32_e32 v251, 0xffff0000, v105
	v_fma_f32 v224, v56, v224, v248
	v_fma_f32 v225, v57, v225, v249
	v_fma_f32 v226, v58, v226, v250
	v_fma_f32 v227, v59, v227, v251
	v_mul_f32_e32 v220, v220, v56
	v_mul_f32_e32 v221, v221, v57
	v_mul_f32_e32 v222, v222, v58
	v_mul_f32_e32 v223, v223, v59
	s_waitcnt vmcnt(10)
	v_lshlrev_b32_e32 v248, 16, v106
	v_and_b32_e32 v249, 0xffff0000, v106
	v_lshlrev_b32_e32 v250, 16, v107
	v_and_b32_e32 v251, 0xffff0000, v107
	v_fma_f32 v224, v60, v224, v248
	v_fma_f32 v225, v61, v225, v249
	v_fma_f32 v226, v62, v226, v250
	v_fma_f32 v227, v63, v227, v251
	v_mul_f32_e32 v220, v220, v60
	v_mul_f32_e32 v221, v221, v61
	v_mul_f32_e32 v222, v222, v62
	v_mul_f32_e32 v223, v223, v63
	s_waitcnt vmcnt(8)
	v_lshlrev_b32_e32 v248, 16, v108
	v_and_b32_e32 v249, 0xffff0000, v108
	v_lshlrev_b32_e32 v250, 16, v109
	v_and_b32_e32 v251, 0xffff0000, v109
	v_fma_f32 v224, v64, v224, v248
	v_fma_f32 v225, v65, v225, v249
	v_fma_f32 v226, v66, v226, v250
	v_fma_f32 v227, v67, v227, v251
	v_mul_f32_e32 v220, v220, v64
	v_mul_f32_e32 v221, v221, v65
	v_mul_f32_e32 v222, v222, v66
	v_mul_f32_e32 v223, v223, v67
	s_waitcnt vmcnt(6)
	v_lshlrev_b32_e32 v248, 16, v110
	v_and_b32_e32 v249, 0xffff0000, v110
	v_lshlrev_b32_e32 v250, 16, v111
	v_and_b32_e32 v251, 0xffff0000, v111
	v_fma_f32 v224, v68, v224, v248
	v_fma_f32 v225, v69, v225, v249
	v_fma_f32 v226, v70, v226, v250
	v_fma_f32 v227, v71, v227, v251
	v_mul_f32_e32 v220, v220, v68
	v_mul_f32_e32 v221, v221, v69
	v_mul_f32_e32 v222, v222, v70
	v_mul_f32_e32 v223, v223, v71
	s_waitcnt vmcnt(4)
	v_lshlrev_b32_e32 v248, 16, v112
	v_and_b32_e32 v249, 0xffff0000, v112
	v_lshlrev_b32_e32 v250, 16, v113
	v_and_b32_e32 v251, 0xffff0000, v113
	v_fma_f32 v224, v72, v224, v248
	v_fma_f32 v225, v73, v225, v249
	v_fma_f32 v226, v74, v226, v250
	v_fma_f32 v227, v75, v227, v251
	v_mul_f32_e32 v220, v220, v72
	v_mul_f32_e32 v221, v221, v73
	v_mul_f32_e32 v222, v222, v74
	v_mul_f32_e32 v223, v223, v75
	s_waitcnt vmcnt(2)
	v_lshlrev_b32_e32 v248, 16, v114
	v_and_b32_e32 v249, 0xffff0000, v114
	v_lshlrev_b32_e32 v250, 16, v115
	v_and_b32_e32 v251, 0xffff0000, v115
	v_fma_f32 v224, v76, v224, v248
	v_fma_f32 v225, v77, v225, v249
	v_fma_f32 v226, v78, v226, v250
	v_fma_f32 v227, v79, v227, v251
	v_mul_f32_e32 v220, v220, v76
	v_mul_f32_e32 v221, v221, v77
	v_mul_f32_e32 v222, v222, v78
	v_mul_f32_e32 v223, v223, v79
	s_waitcnt vmcnt(0)
	v_lshlrev_b32_e32 v248, 16, v116
	v_and_b32_e32 v249, 0xffff0000, v116
	v_lshlrev_b32_e32 v250, 16, v117
	v_and_b32_e32 v251, 0xffff0000, v117
	v_fma_f32 v224, v80, v224, v248
	v_fma_f32 v225, v81, v225, v249
	v_fma_f32 v226, v82, v226, v250
	v_fma_f32 v227, v83, v227, v251
	v_mul_f32_e32 v220, v220, v80
	v_mul_f32_e32 v221, v221, v81
	v_mul_f32_e32 v222, v222, v82
	v_mul_f32_e32 v223, v223, v83
	v_cmp_lt_u32_e32 vcc, 0, v6
	v_cmp_lt_u32_e64 s[36:37], 1, v6
	s_nop 0
	v_cndmask_b32_e32 v248, v12, v11, vcc
	v_cndmask_b32_e64 v249, v12, v11, s[36:37]
	v_add_u32_e32 v249, 0x800, v249
	global_load_dwordx4 v[118:121], v248, s[58:59]
	global_load_dwordx4 v[122:125], v249, s[58:59]
	v_cmp_lt_u32_e32 vcc, 0, v6
	v_cmp_lt_u32_e64 s[36:37], 1, v6
	s_nop 0
	v_cndmask_b32_e32 v250, v14, v13, vcc
	v_cndmask_b32_e64 v251, v14, v13, s[36:37]
	v_add_u32_e32 v251, 0x1400, v251
	global_load_dwordx2 v[186:187], v250, s[52:53]
	global_load_dwordx2 v[188:189], v251, s[52:53]
	v_cmp_lt_u32_e32 vcc, 2, v6
	v_cmp_lt_u32_e64 s[36:37], 3, v6
	s_nop 0
	v_cndmask_b32_e32 v248, v12, v11, vcc
	v_cndmask_b32_e64 v249, v12, v11, s[36:37]
	v_add_u32_e32 v248, 0x1000, v248
	v_add_u32_e32 v249, 0x1800, v249
	global_load_dwordx4 v[126:129], v248, s[58:59]
	global_load_dwordx4 v[130:133], v249, s[58:59]
	v_cmp_lt_u32_e32 vcc, 2, v6
	v_cmp_lt_u32_e64 s[36:37], 3, v6
	s_nop 0
	v_cndmask_b32_e32 v250, v14, v13, vcc
	v_cndmask_b32_e64 v251, v14, v13, s[36:37]
	v_add_u32_e32 v250, 0x2800, v250
	v_add_u32_e32 v251, 0x3c00, v251
	global_load_dwordx2 v[190:191], v250, s[52:53]
	global_load_dwordx2 v[192:193], v251, s[52:53]
	v_cmp_lt_u32_e32 vcc, 4, v6
	v_cmp_lt_u32_e64 s[36:37], 5, v6
	s_nop 0
	v_cndmask_b32_e32 v248, v12, v11, vcc
	v_cndmask_b32_e64 v249, v12, v11, s[36:37]
	v_add_u32_e32 v248, 0x2000, v248
	v_add_u32_e32 v249, 0x2800, v249
	global_load_dwordx4 v[134:137], v248, s[58:59]
	global_load_dwordx4 v[138:141], v249, s[58:59]
	v_cmp_lt_u32_e32 vcc, 4, v6
	v_cmp_lt_u32_e64 s[36:37], 5, v6
	s_nop 0
	v_cndmask_b32_e32 v250, v14, v13, vcc
	v_cndmask_b32_e64 v251, v14, v13, s[36:37]
	v_add_u32_e32 v250, 0x5000, v250
	v_add_u32_e32 v251, 0x6400, v251
	global_load_dwordx2 v[194:195], v250, s[52:53]
	global_load_dwordx2 v[196:197], v251, s[52:53]
	v_cmp_lt_u32_e32 vcc, 6, v6
	v_cmp_lt_u32_e64 s[36:37], 7, v6
	s_nop 0
	v_cndmask_b32_e32 v248, v12, v11, vcc
	v_cndmask_b32_e64 v249, v12, v11, s[36:37]
	v_add_u32_e32 v248, 0x3000, v248
	v_add_u32_e32 v249, 0x3800, v249
	global_load_dwordx4 v[142:145], v248, s[58:59]
	global_load_dwordx4 v[146:149], v249, s[58:59]
	v_cmp_lt_u32_e32 vcc, 6, v6
	v_cmp_lt_u32_e64 s[36:37], 7, v6
	s_nop 0
	v_cndmask_b32_e32 v250, v14, v13, vcc
	v_cndmask_b32_e64 v251, v14, v13, s[36:37]
	v_add_u32_e32 v250, 0x7800, v250
	v_add_u32_e32 v251, 0x8c00, v251
	global_load_dwordx2 v[198:199], v250, s[52:53]
	global_load_dwordx2 v[200:201], v251, s[52:53]
	v_cmp_lt_u32_e32 vcc, 8, v6
	v_cmp_lt_u32_e64 s[36:37], 9, v6
	s_nop 0
	v_cndmask_b32_e32 v248, v12, v11, vcc
	v_cndmask_b32_e64 v249, v12, v11, s[36:37]
	v_add_u32_e32 v248, 0x4000, v248
	v_add_u32_e32 v249, 0x4800, v249
	global_load_dwordx4 v[150:153], v248, s[58:59]
	global_load_dwordx4 v[154:157], v249, s[58:59]
	v_cmp_lt_u32_e32 vcc, 8, v6
	v_cmp_lt_u32_e64 s[36:37], 9, v6
	s_nop 0
	v_cndmask_b32_e32 v250, v14, v13, vcc
	v_cndmask_b32_e64 v251, v14, v13, s[36:37]
	v_add_u32_e32 v250, 0xa000, v250
	v_add_u32_e32 v251, 0xb400, v251
	global_load_dwordx2 v[202:203], v250, s[52:53]
	global_load_dwordx2 v[204:205], v251, s[52:53]
	v_cmp_lt_u32_e32 vcc, 10, v6
	v_cmp_lt_u32_e64 s[36:37], 11, v6
	s_nop 0
	v_cndmask_b32_e32 v248, v12, v11, vcc
	v_cndmask_b32_e64 v249, v12, v11, s[36:37]
	v_add_u32_e32 v248, 0x5000, v248
	v_add_u32_e32 v249, 0x5800, v249
	global_load_dwordx4 v[158:161], v248, s[58:59]
	global_load_dwordx4 v[162:165], v249, s[58:59]
	v_cmp_lt_u32_e32 vcc, 10, v6
	v_cmp_lt_u32_e64 s[36:37], 11, v6
	s_nop 0
	v_cndmask_b32_e32 v250, v14, v13, vcc
	v_cndmask_b32_e64 v251, v14, v13, s[36:37]
	v_add_u32_e32 v250, 0xc800, v250
	v_add_u32_e32 v251, 0xdc00, v251
	global_load_dwordx2 v[206:207], v250, s[52:53]
	global_load_dwordx2 v[208:209], v251, s[52:53]
	v_cmp_lt_u32_e32 vcc, 12, v6
	v_cmp_lt_u32_e64 s[36:37], 13, v6
	s_nop 0
	v_cndmask_b32_e32 v248, v12, v11, vcc
	v_cndmask_b32_e64 v249, v12, v11, s[36:37]
	v_add_u32_e32 v248, 0x6000, v248
	v_add_u32_e32 v249, 0x6800, v249
	global_load_dwordx4 v[166:169], v248, s[58:59]
	global_load_dwordx4 v[170:173], v249, s[58:59]
	v_cmp_lt_u32_e32 vcc, 12, v6
	v_cmp_lt_u32_e64 s[36:37], 13, v6
	s_nop 0
	v_cndmask_b32_e32 v250, v14, v13, vcc
	v_cndmask_b32_e64 v251, v14, v13, s[36:37]
	v_add_u32_e32 v250, 0xf000, v250
	v_add_u32_e32 v251, 0x10400, v251
	global_load_dwordx2 v[210:211], v250, s[52:53]
	global_load_dwordx2 v[212:213], v251, s[52:53]
	v_cmp_lt_u32_e32 vcc, 14, v6
	v_cmp_lt_u32_e64 s[36:37], 15, v6
	s_nop 0
	v_cndmask_b32_e32 v248, v12, v11, vcc
	v_cndmask_b32_e64 v249, v12, v11, s[36:37]
	v_add_u32_e32 v248, 0x7000, v248
	v_add_u32_e32 v249, 0x7800, v249
	global_load_dwordx4 v[174:177], v248, s[58:59]
	global_load_dwordx4 v[178:181], v249, s[58:59]
	v_cmp_lt_u32_e32 vcc, 14, v6
	v_cmp_lt_u32_e64 s[36:37], 15, v6
	s_nop 0
	v_cndmask_b32_e32 v250, v14, v13, vcc
	v_cndmask_b32_e64 v251, v14, v13, s[36:37]
	v_add_u32_e32 v250, 0x11800, v250
	v_add_u32_e32 v251, 0x12c00, v251
	global_load_dwordx2 v[214:215], v250, s[52:53]
	global_load_dwordx2 v[216:217], v251, s[52:53]
	v_cmp_lt_u32_e32 vcc, 16, v6
	s_nop 1
	v_cndmask_b32_e32 v248, v12, v11, vcc
	v_add_u32_e32 v248, 0x8000, v248
	global_load_dwordx4 v[182:185], v248, s[58:59]
	v_cmp_lt_u32_e32 vcc, 16, v6
	s_nop 1
	v_cndmask_b32_e32 v250, v14, v13, vcc
	v_add_u32_e32 v250, 0x14000, v250
	global_load_dwordx2 v[218:219], v250, s[52:53]
	v_cmp_le_u32_e32 vcc, 2, v1
	v_add_u32_e32 v252, 0xfffffff8, v7
	ds_bpermute_b32 v228, v252, v220
	ds_bpermute_b32 v229, v252, v221
	ds_bpermute_b32 v230, v252, v222
	ds_bpermute_b32 v231, v252, v223
	ds_bpermute_b32 v232, v252, v224
	ds_bpermute_b32 v233, v252, v225
	ds_bpermute_b32 v234, v252, v226
	ds_bpermute_b32 v235, v252, v227
	s_waitcnt lgkmcnt(0)
	v_fma_f32 v248, v220, v232, v224
	v_fma_f32 v249, v221, v233, v225
	v_fma_f32 v250, v222, v234, v226
	v_fma_f32 v251, v223, v235, v227
	v_mul_f32_e32 v228, v220, v228
	v_mul_f32_e32 v229, v221, v229
	v_mul_f32_e32 v230, v222, v230
	v_mul_f32_e32 v231, v223, v231
	v_cndmask_b32_e32 v224, v224, v248, vcc
	v_cndmask_b32_e32 v225, v225, v249, vcc
	v_cndmask_b32_e32 v226, v226, v250, vcc
	v_cndmask_b32_e32 v227, v227, v251, vcc
	v_cndmask_b32_e32 v220, v220, v228, vcc
	v_cndmask_b32_e32 v221, v221, v229, vcc
	v_cndmask_b32_e32 v222, v222, v230, vcc
	v_cndmask_b32_e32 v223, v223, v231, vcc
	v_cmp_le_u32_e32 vcc, 4, v1
	v_add_u32_e32 v252, 0xfffffff0, v7
	ds_bpermute_b32 v228, v252, v220
	ds_bpermute_b32 v229, v252, v221
	ds_bpermute_b32 v230, v252, v222
	ds_bpermute_b32 v231, v252, v223
	ds_bpermute_b32 v232, v252, v224
	ds_bpermute_b32 v233, v252, v225
	ds_bpermute_b32 v234, v252, v226
	ds_bpermute_b32 v235, v252, v227
	s_waitcnt lgkmcnt(0)
	v_fma_f32 v248, v220, v232, v224
	v_fma_f32 v249, v221, v233, v225
	v_fma_f32 v250, v222, v234, v226
	v_fma_f32 v251, v223, v235, v227
	v_mul_f32_e32 v228, v220, v228
	v_mul_f32_e32 v229, v221, v229
	v_mul_f32_e32 v230, v222, v230
	v_mul_f32_e32 v231, v223, v231
	v_cndmask_b32_e32 v224, v224, v248, vcc
	v_cndmask_b32_e32 v225, v225, v249, vcc
	v_cndmask_b32_e32 v226, v226, v250, vcc
	v_cndmask_b32_e32 v227, v227, v251, vcc
	v_cndmask_b32_e32 v220, v220, v228, vcc
	v_cndmask_b32_e32 v221, v221, v229, vcc
	v_cndmask_b32_e32 v222, v222, v230, vcc
	v_cndmask_b32_e32 v223, v223, v231, vcc
	v_cmp_le_u32_e32 vcc, 8, v1
	v_add_u32_e32 v252, 0xffffffe0, v7
	ds_bpermute_b32 v228, v252, v220
	ds_bpermute_b32 v229, v252, v221
	ds_bpermute_b32 v230, v252, v222
	ds_bpermute_b32 v231, v252, v223
	ds_bpermute_b32 v232, v252, v224
	ds_bpermute_b32 v233, v252, v225
	ds_bpermute_b32 v234, v252, v226
	ds_bpermute_b32 v235, v252, v227
	s_waitcnt lgkmcnt(0)
	v_fma_f32 v248, v220, v232, v224
	v_fma_f32 v249, v221, v233, v225
	v_fma_f32 v250, v222, v234, v226
	v_fma_f32 v251, v223, v235, v227
	v_mul_f32_e32 v228, v220, v228
	v_mul_f32_e32 v229, v221, v229
	v_mul_f32_e32 v230, v222, v230
	v_mul_f32_e32 v231, v223, v231
	v_cndmask_b32_e32 v224, v224, v248, vcc
	v_cndmask_b32_e32 v225, v225, v249, vcc
	v_cndmask_b32_e32 v226, v226, v250, vcc
	v_cndmask_b32_e32 v227, v227, v251, vcc
	v_cndmask_b32_e32 v220, v220, v228, vcc
	v_cndmask_b32_e32 v221, v221, v229, vcc
	v_cndmask_b32_e32 v222, v222, v230, vcc
	v_cndmask_b32_e32 v223, v223, v231, vcc
	v_cmp_le_u32_e32 vcc, 16, v1
	v_add_u32_e32 v252, 0xffffffc0, v7
	ds_bpermute_b32 v228, v252, v220
	ds_bpermute_b32 v229, v252, v221
	ds_bpermute_b32 v230, v252, v222
	ds_bpermute_b32 v231, v252, v223
	ds_bpermute_b32 v232, v252, v224
	ds_bpermute_b32 v233, v252, v225
	ds_bpermute_b32 v234, v252, v226
	ds_bpermute_b32 v235, v252, v227
	s_waitcnt lgkmcnt(0)
	v_fma_f32 v248, v220, v232, v224
	v_fma_f32 v249, v221, v233, v225
	v_fma_f32 v250, v222, v234, v226
	v_fma_f32 v251, v223, v235, v227
	v_mul_f32_e32 v228, v220, v228
	v_mul_f32_e32 v229, v221, v229
	v_mul_f32_e32 v230, v222, v230
	v_mul_f32_e32 v231, v223, v231
	v_cndmask_b32_e32 v224, v224, v248, vcc
	v_cndmask_b32_e32 v225, v225, v249, vcc
	v_cndmask_b32_e32 v226, v226, v250, vcc
	v_cndmask_b32_e32 v227, v227, v251, vcc
	v_cndmask_b32_e32 v220, v220, v228, vcc
	v_cndmask_b32_e32 v221, v221, v229, vcc
	v_cndmask_b32_e32 v222, v222, v230, vcc
	v_cndmask_b32_e32 v223, v223, v231, vcc
	v_cmp_le_u32_e32 vcc, 32, v1
	v_add_u32_e32 v252, 0xffffff80, v7
	ds_bpermute_b32 v228, v252, v220
	ds_bpermute_b32 v229, v252, v221
	ds_bpermute_b32 v230, v252, v222
	ds_bpermute_b32 v231, v252, v223
	ds_bpermute_b32 v232, v252, v224
	ds_bpermute_b32 v233, v252, v225
	ds_bpermute_b32 v234, v252, v226
	ds_bpermute_b32 v235, v252, v227
	s_waitcnt lgkmcnt(0)
	v_fma_f32 v248, v220, v232, v224
	v_fma_f32 v249, v221, v233, v225
	v_fma_f32 v250, v222, v234, v226
	v_fma_f32 v251, v223, v235, v227
	v_mul_f32_e32 v228, v220, v228
	v_mul_f32_e32 v229, v221, v229
	v_mul_f32_e32 v230, v222, v230
	v_mul_f32_e32 v231, v223, v231
	v_cndmask_b32_e32 v224, v224, v248, vcc
	v_cndmask_b32_e32 v225, v225, v249, vcc
	v_cndmask_b32_e32 v226, v226, v250, vcc
	v_cndmask_b32_e32 v227, v227, v251, vcc
	v_cndmask_b32_e32 v220, v220, v228, vcc
	v_cndmask_b32_e32 v221, v221, v229, vcc
	v_cndmask_b32_e32 v222, v222, v230, vcc
	v_cndmask_b32_e32 v223, v223, v231, vcc
	v_cmp_lt_u32_e32 vcc, 61, v1
	s_lshl_b32 s13, s12, 6
	v_add_u32_e32 v252, s13, v8
	s_and_saveexec_b64 s[38:39], vcc
	ds_write_b128 v252, v[220:223]
	ds_write_b128 v252, v[224:227] offset:16
	s_or_b64 exec, exec, s[38:39]
	s_waitcnt lgkmcnt(0)
	s_barrier
	v_mov_b32_e32 v244, 0
	v_mov_b32_e32 v245, 0
	v_mov_b32_e32 v246, 0
	v_mov_b32_e32 v247, 0
	ds_read_b128 v[228:231], v8 offset:0
	ds_read_b128 v[232:235], v8 offset:16
	ds_read_b128 v[236:239], v8 offset:64
	ds_read_b128 v[240:243], v8 offset:80
	s_cmp_le_u32 s12, 0
	s_cbranch_scc1 .Lrg_cdone1
	s_waitcnt lgkmcnt(2)
	v_fma_f32 v244, v228, v244, v232
	v_fma_f32 v245, v229, v245, v233
	v_fma_f32 v246, v230, v246, v234
	v_fma_f32 v247, v231, v247, v235
	ds_read_b128 v[228:231], v8 offset:128
	ds_read_b128 v[232:235], v8 offset:144
	s_cmp_le_u32 s12, 1
	s_cbranch_scc1 .Lrg_cdone1
	s_waitcnt lgkmcnt(2)
	v_fma_f32 v244, v236, v244, v240
	v_fma_f32 v245, v237, v245, v241
	v_fma_f32 v246, v238, v246, v242
	v_fma_f32 v247, v239, v247, v243
	ds_read_b128 v[236:239], v8 offset:192
	ds_read_b128 v[240:243], v8 offset:208
	s_cmp_le_u32 s12, 2
	s_cbranch_scc1 .Lrg_cdone1
	s_waitcnt lgkmcnt(2)
	v_fma_f32 v244, v228, v244, v232
	v_fma_f32 v245, v229, v245, v233
	v_fma_f32 v246, v230, v246, v234
	v_fma_f32 v247, v231, v247, v235
	ds_read_b128 v[228:231], v8 offset:256
	ds_read_b128 v[232:235], v8 offset:272
	s_cmp_le_u32 s12, 3
	s_cbranch_scc1 .Lrg_cdone1
	s_waitcnt lgkmcnt(2)
	v_fma_f32 v244, v236, v244, v240
	v_fma_f32 v245, v237, v245, v241
	v_fma_f32 v246, v238, v246, v242
	v_fma_f32 v247, v239, v247, v243
	ds_read_b128 v[236:239], v8 offset:320
	ds_read_b128 v[240:243], v8 offset:336
	s_cmp_le_u32 s12, 4
	s_cbranch_scc1 .Lrg_cdone1
	s_waitcnt lgkmcnt(2)
	v_fma_f32 v244, v228, v244, v232
	v_fma_f32 v245, v229, v245, v233
	v_fma_f32 v246, v230, v246, v234
	v_fma_f32 v247, v231, v247, v235
	ds_read_b128 v[228:231], v8 offset:384
	ds_read_b128 v[232:235], v8 offset:400
	s_cmp_le_u32 s12, 5
	s_cbranch_scc1 .Lrg_cdone1
	s_waitcnt lgkmcnt(2)
	v_fma_f32 v244, v236, v244, v240
	v_fma_f32 v245, v237, v245, v241
	v_fma_f32 v246, v238, v246, v242
	v_fma_f32 v247, v239, v247, v243
	s_cmp_le_u32 s12, 6
	s_cbranch_scc1 .Lrg_cdone1
	s_waitcnt lgkmcnt(0)
	v_fma_f32 v244, v228, v244, v232
	v_fma_f32 v245, v229, v245, v233
	v_fma_f32 v246, v230, v246, v234
	v_fma_f32 v247, v231, v247, v235
.Lrg_cdone1:
	s_waitcnt lgkmcnt(0)
	v_cmp_le_u32_e32 vcc, 2, v1
	v_add_u32_e32 v252, -8, v7
	ds_bpermute_b32 v228, v252, v220
	ds_bpermute_b32 v229, v252, v221
	ds_bpermute_b32 v230, v252, v222
	ds_bpermute_b32 v231, v252, v223
	ds_bpermute_b32 v232, v252, v224
	ds_bpermute_b32 v233, v252, v225
	ds_bpermute_b32 v234, v252, v226
	ds_bpermute_b32 v235, v252, v227
	s_waitcnt lgkmcnt(0)
	v_fma_f32 v248, v228, v244, v232
	v_fma_f32 v249, v229, v245, v233
	v_fma_f32 v250, v230, v246, v234
	v_fma_f32 v251, v231, v247, v235
	v_cndmask_b32_e32 v244, v244, v248, vcc
	v_cndmask_b32_e32 v245, v245, v249, vcc
	v_cndmask_b32_e32 v246, v246, v250, vcc
	v_cndmask_b32_e32 v247, v247, v251, vcc
	s_waitcnt vmcnt(31)
	v_lshlrev_b32_e32 v248, 16, v84
	v_and_b32_e32 v249, 0xffff0000, v84
	v_lshlrev_b32_e32 v250, 16, v85
	v_and_b32_e32 v251, 0xffff0000, v85
	v_fma_f32 v16, v16, v244, v248
	v_fma_f32 v17, v17, v245, v249
	v_fma_f32 v18, v18, v246, v250
	v_fma_f32 v19, v19, v247, v251
	v_cmp_lt_u32_e32 vcc, 0, v6
	v_add_f32_e32 v118, v16, v118
	v_add_f32_e32 v119, v17, v119
	v_add_f32_e32 v120, v18, v120
	v_add_f32_e32 v121, v19, v121
	v_cndmask_b32_e32 v252, v12, v11, vcc
	v_lshlrev_b32_e32 v248, 16, v186
	v_and_b32_e32 v249, 0xffff0000, v186
	v_lshlrev_b32_e32 v250, 16, v187
	v_and_b32_e32 v251, 0xffff0000, v187
	v_mul_f32_e32 v228, 0x3d372713, v248
	v_mul_f32_e32 v229, 0x3d372713, v249
	v_mul_f32_e32 v230, 0x3d372713, v250
	v_mul_f32_e32 v231, 0x3d372713, v251
	v_mul_f32_e32 v228, v228, v248
	v_mul_f32_e32 v229, v229, v249
	v_mul_f32_e32 v230, v230, v250
	v_mul_f32_e32 v231, v231, v251
	v_fma_f32 v228, v228, v248, v248
	v_fma_f32 v229, v229, v249, v249
	v_fma_f32 v230, v230, v250, v250
	v_fma_f32 v231, v231, v251, v251
	v_mul_f32_e32 v228, 0x40135761, v228
	v_mul_f32_e32 v229, 0x40135761, v229
	v_mul_f32_e32 v230, 0x40135761, v230
	v_mul_f32_e32 v231, 0x40135761, v231
	v_exp_f32_e32 v228, v228
	v_exp_f32_e32 v229, v229
	v_exp_f32_e32 v230, v230
	v_exp_f32_e32 v231, v231
	s_nop 0
	v_add_f32_e32 v228, 1.0, v228
	v_add_f32_e32 v229, 1.0, v229
	v_add_f32_e32 v230, 1.0, v230
	v_add_f32_e32 v231, 1.0, v231
	v_rcp_f32_e32 v228, v228
	v_rcp_f32_e32 v229, v229
	v_rcp_f32_e32 v230, v230
	v_rcp_f32_e32 v231, v231
	v_add_u32_e32 v252, v252, v15
	v_sub_f32_e32 v228, 1.0, v228
	v_sub_f32_e32 v229, 1.0, v229
	v_sub_f32_e32 v230, 1.0, v230
	v_sub_f32_e32 v231, 1.0, v231
	v_mul_f32_e32 v228, v228, v248
	v_mul_f32_e32 v229, v229, v249
	v_mul_f32_e32 v230, v230, v250
	v_mul_f32_e32 v231, v231, v251
	v_mul_f32_e32 v228, v118, v228
	v_mul_f32_e32 v229, v119, v229
	v_mul_f32_e32 v230, v120, v230
	v_mul_f32_e32 v231, v121, v231
	v_cvt_pk_bf16_f32 v118, v228, v229
	v_cvt_pk_bf16_f32 v119, v230, v231
	global_store_dwordx2 v252, v[118:119], s[54:55]
	s_waitcnt vmcnt(31)
	v_lshlrev_b32_e32 v248, 16, v86
	v_and_b32_e32 v249, 0xffff0000, v86
	v_lshlrev_b32_e32 v250, 16, v87
	v_and_b32_e32 v251, 0xffff0000, v87
	v_fma_f32 v20, v20, v16, v248
	v_fma_f32 v21, v21, v17, v249
	v_fma_f32 v22, v22, v18, v250
	v_fma_f32 v23, v23, v19, v251
	v_cmp_lt_u32_e32 vcc, 1, v6
	v_add_f32_e32 v122, v20, v122
	v_add_f32_e32 v123, v21, v123
	v_add_f32_e32 v124, v22, v124
	v_add_f32_e32 v125, v23, v125
	v_cndmask_b32_e32 v252, v12, v11, vcc
	v_lshlrev_b32_e32 v248, 16, v188
	v_and_b32_e32 v249, 0xffff0000, v188
	v_lshlrev_b32_e32 v250, 16, v189
	v_and_b32_e32 v251, 0xffff0000, v189
	v_mul_f32_e32 v228, 0x3d372713, v248
	v_mul_f32_e32 v229, 0x3d372713, v249
	v_mul_f32_e32 v230, 0x3d372713, v250
	v_mul_f32_e32 v231, 0x3d372713, v251
	v_mul_f32_e32 v228, v228, v248
	v_mul_f32_e32 v229, v229, v249
	v_mul_f32_e32 v230, v230, v250
	v_mul_f32_e32 v231, v231, v251
	v_fma_f32 v228, v228, v248, v248
	v_fma_f32 v229, v229, v249, v249
	v_fma_f32 v230, v230, v250, v250
	v_fma_f32 v231, v231, v251, v251
	v_mul_f32_e32 v228, 0x40135761, v228
	v_mul_f32_e32 v229, 0x40135761, v229
	v_mul_f32_e32 v230, 0x40135761, v230
	v_mul_f32_e32 v231, 0x40135761, v231
	v_exp_f32_e32 v228, v228
	v_exp_f32_e32 v229, v229
	v_exp_f32_e32 v230, v230
	v_exp_f32_e32 v231, v231
	v_add_u32_e32 v252, 0x800, v252
	v_add_f32_e32 v228, 1.0, v228
	v_add_f32_e32 v229, 1.0, v229
	v_add_f32_e32 v230, 1.0, v230
	v_add_f32_e32 v231, 1.0, v231
	v_rcp_f32_e32 v228, v228
	v_rcp_f32_e32 v229, v229
	v_rcp_f32_e32 v230, v230
	v_rcp_f32_e32 v231, v231
	v_add_u32_e32 v252, v252, v15
	v_sub_f32_e32 v228, 1.0, v228
	v_sub_f32_e32 v229, 1.0, v229
	v_sub_f32_e32 v230, 1.0, v230
	v_sub_f32_e32 v231, 1.0, v231
	v_mul_f32_e32 v228, v228, v248
	v_mul_f32_e32 v229, v229, v249
	v_mul_f32_e32 v230, v230, v250
	v_mul_f32_e32 v231, v231, v251
	v_mul_f32_e32 v228, v122, v228
	v_mul_f32_e32 v229, v123, v229
	v_mul_f32_e32 v230, v124, v230
	v_mul_f32_e32 v231, v125, v231
	v_cvt_pk_bf16_f32 v122, v228, v229
	v_cvt_pk_bf16_f32 v123, v230, v231
	global_store_dwordx2 v252, v[122:123], s[54:55]
	s_waitcnt vmcnt(29)
	v_lshlrev_b32_e32 v248, 16, v88
	v_and_b32_e32 v249, 0xffff0000, v88
	v_lshlrev_b32_e32 v250, 16, v89
	v_and_b32_e32 v251, 0xffff0000, v89
	v_fma_f32 v24, v24, v20, v248
	v_fma_f32 v25, v25, v21, v249
	v_fma_f32 v26, v26, v22, v250
	v_fma_f32 v27, v27, v23, v251
	v_cmp_lt_u32_e32 vcc, 2, v6
	v_add_f32_e32 v126, v24, v126
	v_add_f32_e32 v127, v25, v127
	v_add_f32_e32 v128, v26, v128
	v_add_f32_e32 v129, v27, v129
	v_cndmask_b32_e32 v252, v12, v11, vcc
	v_lshlrev_b32_e32 v248, 16, v190
	v_and_b32_e32 v249, 0xffff0000, v190
	v_lshlrev_b32_e32 v250, 16, v191
	v_and_b32_e32 v251, 0xffff0000, v191
	v_mul_f32_e32 v228, 0x3d372713, v248
	v_mul_f32_e32 v229, 0x3d372713, v249
	v_mul_f32_e32 v230, 0x3d372713, v250
	v_mul_f32_e32 v231, 0x3d372713, v251
	v_mul_f32_e32 v228, v228, v248
	v_mul_f32_e32 v229, v229, v249
	v_mul_f32_e32 v230, v230, v250
	v_mul_f32_e32 v231, v231, v251
	v_fma_f32 v228, v228, v248, v248
	v_fma_f32 v229, v229, v249, v249
	v_fma_f32 v230, v230, v250, v250
	v_fma_f32 v231, v231, v251, v251
	v_mul_f32_e32 v228, 0x40135761, v228
	v_mul_f32_e32 v229, 0x40135761, v229
	v_mul_f32_e32 v230, 0x40135761, v230
	v_mul_f32_e32 v231, 0x40135761, v231
	v_exp_f32_e32 v228, v228
	v_exp_f32_e32 v229, v229
	v_exp_f32_e32 v230, v230
	v_exp_f32_e32 v231, v231
	v_add_u32_e32 v252, 0x1000, v252
	v_add_f32_e32 v228, 1.0, v228
	v_add_f32_e32 v229, 1.0, v229
	v_add_f32_e32 v230, 1.0, v230
	v_add_f32_e32 v231, 1.0, v231
	v_rcp_f32_e32 v228, v228
	v_rcp_f32_e32 v229, v229
	v_rcp_f32_e32 v230, v230
	v_rcp_f32_e32 v231, v231
	v_add_u32_e32 v252, v252, v15
	v_sub_f32_e32 v228, 1.0, v228
	v_sub_f32_e32 v229, 1.0, v229
	v_sub_f32_e32 v230, 1.0, v230
	v_sub_f32_e32 v231, 1.0, v231
	v_mul_f32_e32 v228, v228, v248
	v_mul_f32_e32 v229, v229, v249
	v_mul_f32_e32 v230, v230, v250
	v_mul_f32_e32 v231, v231, v251
	v_mul_f32_e32 v228, v126, v228
	v_mul_f32_e32 v229, v127, v229
	v_mul_f32_e32 v230, v128, v230
	v_mul_f32_e32 v231, v129, v231
	v_cvt_pk_bf16_f32 v126, v228, v229
	v_cvt_pk_bf16_f32 v127, v230, v231
	global_store_dwordx2 v252, v[126:127], s[54:55]
	s_waitcnt vmcnt(29)
	v_lshlrev_b32_e32 v248, 16, v90
	v_and_b32_e32 v249, 0xffff0000, v90
	v_lshlrev_b32_e32 v250, 16, v91
	v_and_b32_e32 v251, 0xffff0000, v91
	v_fma_f32 v28, v28, v24, v248
	v_fma_f32 v29, v29, v25, v249
	v_fma_f32 v30, v30, v26, v250
	v_fma_f32 v31, v31, v27, v251
	v_cmp_lt_u32_e32 vcc, 3, v6
	v_add_f32_e32 v130, v28, v130
	v_add_f32_e32 v131, v29, v131
	v_add_f32_e32 v132, v30, v132
	v_add_f32_e32 v133, v31, v133
	v_cndmask_b32_e32 v252, v12, v11, vcc
	v_lshlrev_b32_e32 v248, 16, v192
	v_and_b32_e32 v249, 0xffff0000, v192
	v_lshlrev_b32_e32 v250, 16, v193
	v_and_b32_e32 v251, 0xffff0000, v193
	v_mul_f32_e32 v228, 0x3d372713, v248
	v_mul_f32_e32 v229, 0x3d372713, v249
	v_mul_f32_e32 v230, 0x3d372713, v250
	v_mul_f32_e32 v231, 0x3d372713, v251
	v_mul_f32_e32 v228, v228, v248
	v_mul_f32_e32 v229, v229, v249
	v_mul_f32_e32 v230, v230, v250
	v_mul_f32_e32 v231, v231, v251
	v_fma_f32 v228, v228, v248, v248
	v_fma_f32 v229, v229, v249, v249
	v_fma_f32 v230, v230, v250, v250
	v_fma_f32 v231, v231, v251, v251
	v_mul_f32_e32 v228, 0x40135761, v228
	v_mul_f32_e32 v229, 0x40135761, v229
	v_mul_f32_e32 v230, 0x40135761, v230
	v_mul_f32_e32 v231, 0x40135761, v231
	v_exp_f32_e32 v228, v228
	v_exp_f32_e32 v229, v229
	v_exp_f32_e32 v230, v230
	v_exp_f32_e32 v231, v231
	v_add_u32_e32 v252, 0x1800, v252
	v_add_f32_e32 v228, 1.0, v228
	v_add_f32_e32 v229, 1.0, v229
	v_add_f32_e32 v230, 1.0, v230
	v_add_f32_e32 v231, 1.0, v231
	v_rcp_f32_e32 v228, v228
	v_rcp_f32_e32 v229, v229
	v_rcp_f32_e32 v230, v230
	v_rcp_f32_e32 v231, v231
	v_add_u32_e32 v252, v252, v15
	v_sub_f32_e32 v228, 1.0, v228
	v_sub_f32_e32 v229, 1.0, v229
	v_sub_f32_e32 v230, 1.0, v230
	v_sub_f32_e32 v231, 1.0, v231
	v_mul_f32_e32 v228, v228, v248
	v_mul_f32_e32 v229, v229, v249
	v_mul_f32_e32 v230, v230, v250
	v_mul_f32_e32 v231, v231, v251
	v_mul_f32_e32 v228, v130, v228
	v_mul_f32_e32 v229, v131, v229
	v_mul_f32_e32 v230, v132, v230
	v_mul_f32_e32 v231, v133, v231
	v_cvt_pk_bf16_f32 v130, v228, v229
	v_cvt_pk_bf16_f32 v131, v230, v231
	global_store_dwordx2 v252, v[130:131], s[54:55]
	s_waitcnt vmcnt(27)
	v_lshlrev_b32_e32 v248, 16, v92
	v_and_b32_e32 v249, 0xffff0000, v92
	v_lshlrev_b32_e32 v250, 16, v93
	v_and_b32_e32 v251, 0xffff0000, v93
	v_fma_f32 v32, v32, v28, v248
	v_fma_f32 v33, v33, v29, v249
	v_fma_f32 v34, v34, v30, v250
	v_fma_f32 v35, v35, v31, v251
	v_cmp_lt_u32_e32 vcc, 4, v6
	v_add_f32_e32 v134, v32, v134
	v_add_f32_e32 v135, v33, v135
	v_add_f32_e32 v136, v34, v136
	v_add_f32_e32 v137, v35, v137
	v_cndmask_b32_e32 v252, v12, v11, vcc
	v_lshlrev_b32_e32 v248, 16, v194
	v_and_b32_e32 v249, 0xffff0000, v194
	v_lshlrev_b32_e32 v250, 16, v195
	v_and_b32_e32 v251, 0xffff0000, v195
	v_mul_f32_e32 v228, 0x3d372713, v248
	v_mul_f32_e32 v229, 0x3d372713, v249
	v_mul_f32_e32 v230, 0x3d372713, v250
	v_mul_f32_e32 v231, 0x3d372713, v251
	v_mul_f32_e32 v228, v228, v248
	v_mul_f32_e32 v229, v229, v249
	v_mul_f32_e32 v230, v230, v250
	v_mul_f32_e32 v231, v231, v251
	v_fma_f32 v228, v228, v248, v248
	v_fma_f32 v229, v229, v249, v249
	v_fma_f32 v230, v230, v250, v250
	v_fma_f32 v231, v231, v251, v251
	v_mul_f32_e32 v228, 0x40135761, v228
	v_mul_f32_e32 v229, 0x40135761, v229
	v_mul_f32_e32 v230, 0x40135761, v230
	v_mul_f32_e32 v231, 0x40135761, v231
	v_exp_f32_e32 v228, v228
	v_exp_f32_e32 v229, v229
	v_exp_f32_e32 v230, v230
	v_exp_f32_e32 v231, v231
	v_add_u32_e32 v252, 0x2000, v252
	v_add_f32_e32 v228, 1.0, v228
	v_add_f32_e32 v229, 1.0, v229
	v_add_f32_e32 v230, 1.0, v230
	v_add_f32_e32 v231, 1.0, v231
	v_rcp_f32_e32 v228, v228
	v_rcp_f32_e32 v229, v229
	v_rcp_f32_e32 v230, v230
	v_rcp_f32_e32 v231, v231
	v_add_u32_e32 v252, v252, v15
	v_sub_f32_e32 v228, 1.0, v228
	v_sub_f32_e32 v229, 1.0, v229
	v_sub_f32_e32 v230, 1.0, v230
	v_sub_f32_e32 v231, 1.0, v231
	v_mul_f32_e32 v228, v228, v248
	v_mul_f32_e32 v229, v229, v249
	v_mul_f32_e32 v230, v230, v250
	v_mul_f32_e32 v231, v231, v251
	v_mul_f32_e32 v228, v134, v228
	v_mul_f32_e32 v229, v135, v229
	v_mul_f32_e32 v230, v136, v230
	v_mul_f32_e32 v231, v137, v231
	v_cvt_pk_bf16_f32 v134, v228, v229
	v_cvt_pk_bf16_f32 v135, v230, v231
	global_store_dwordx2 v252, v[134:135], s[54:55]
	s_waitcnt vmcnt(27)
	v_lshlrev_b32_e32 v248, 16, v94
	v_and_b32_e32 v249, 0xffff0000, v94
	v_lshlrev_b32_e32 v250, 16, v95
	v_and_b32_e32 v251, 0xffff0000, v95
	v_fma_f32 v36, v36, v32, v248
	v_fma_f32 v37, v37, v33, v249
	v_fma_f32 v38, v38, v34, v250
	v_fma_f32 v39, v39, v35, v251
	v_cmp_lt_u32_e32 vcc, 5, v6
	v_add_f32_e32 v138, v36, v138
	v_add_f32_e32 v139, v37, v139
	v_add_f32_e32 v140, v38, v140
	v_add_f32_e32 v141, v39, v141
	v_cndmask_b32_e32 v252, v12, v11, vcc
	v_lshlrev_b32_e32 v248, 16, v196
	v_and_b32_e32 v249, 0xffff0000, v196
	v_lshlrev_b32_e32 v250, 16, v197
	v_and_b32_e32 v251, 0xffff0000, v197
	v_mul_f32_e32 v228, 0x3d372713, v248
	v_mul_f32_e32 v229, 0x3d372713, v249
	v_mul_f32_e32 v230, 0x3d372713, v250
	v_mul_f32_e32 v231, 0x3d372713, v251
	v_mul_f32_e32 v228, v228, v248
	v_mul_f32_e32 v229, v229, v249
	v_mul_f32_e32 v230, v230, v250
	v_mul_f32_e32 v231, v231, v251
	v_fma_f32 v228, v228, v248, v248
	v_fma_f32 v229, v229, v249, v249
	v_fma_f32 v230, v230, v250, v250
	v_fma_f32 v231, v231, v251, v251
	v_mul_f32_e32 v228, 0x40135761, v228
	v_mul_f32_e32 v229, 0x40135761, v229
	v_mul_f32_e32 v230, 0x40135761, v230
	v_mul_f32_e32 v231, 0x40135761, v231
	v_exp_f32_e32 v228, v228
	v_exp_f32_e32 v229, v229
	v_exp_f32_e32 v230, v230
	v_exp_f32_e32 v231, v231
	v_add_u32_e32 v252, 0x2800, v252
	v_add_f32_e32 v228, 1.0, v228
	v_add_f32_e32 v229, 1.0, v229
	v_add_f32_e32 v230, 1.0, v230
	v_add_f32_e32 v231, 1.0, v231
	v_rcp_f32_e32 v228, v228
	v_rcp_f32_e32 v229, v229
	v_rcp_f32_e32 v230, v230
	v_rcp_f32_e32 v231, v231
	v_add_u32_e32 v252, v252, v15
	v_sub_f32_e32 v228, 1.0, v228
	v_sub_f32_e32 v229, 1.0, v229
	v_sub_f32_e32 v230, 1.0, v230
	v_sub_f32_e32 v231, 1.0, v231
	v_mul_f32_e32 v228, v228, v248
	v_mul_f32_e32 v229, v229, v249
	v_mul_f32_e32 v230, v230, v250
	v_mul_f32_e32 v231, v231, v251
	v_mul_f32_e32 v228, v138, v228
	v_mul_f32_e32 v229, v139, v229
	v_mul_f32_e32 v230, v140, v230
	v_mul_f32_e32 v231, v141, v231
	v_cvt_pk_bf16_f32 v138, v228, v229
	v_cvt_pk_bf16_f32 v139, v230, v231
	global_store_dwordx2 v252, v[138:139], s[54:55]
	s_waitcnt vmcnt(25)
	v_lshlrev_b32_e32 v248, 16, v96
	v_and_b32_e32 v249, 0xffff0000, v96
	v_lshlrev_b32_e32 v250, 16, v97
	v_and_b32_e32 v251, 0xffff0000, v97
	v_fma_f32 v40, v40, v36, v248
	v_fma_f32 v41, v41, v37, v249
	v_fma_f32 v42, v42, v38, v250
	v_fma_f32 v43, v43, v39, v251
	v_cmp_lt_u32_e32 vcc, 6, v6
	v_add_f32_e32 v142, v40, v142
	v_add_f32_e32 v143, v41, v143
	v_add_f32_e32 v144, v42, v144
	v_add_f32_e32 v145, v43, v145
	v_cndmask_b32_e32 v252, v12, v11, vcc
	v_lshlrev_b32_e32 v248, 16, v198
	v_and_b32_e32 v249, 0xffff0000, v198
	v_lshlrev_b32_e32 v250, 16, v199
	v_and_b32_e32 v251, 0xffff0000, v199
	v_mul_f32_e32 v228, 0x3d372713, v248
	v_mul_f32_e32 v229, 0x3d372713, v249
	v_mul_f32_e32 v230, 0x3d372713, v250
	v_mul_f32_e32 v231, 0x3d372713, v251
	v_mul_f32_e32 v228, v228, v248
	v_mul_f32_e32 v229, v229, v249
	v_mul_f32_e32 v230, v230, v250
	v_mul_f32_e32 v231, v231, v251
	v_fma_f32 v228, v228, v248, v248
	v_fma_f32 v229, v229, v249, v249
	v_fma_f32 v230, v230, v250, v250
	v_fma_f32 v231, v231, v251, v251
	v_mul_f32_e32 v228, 0x40135761, v228
	v_mul_f32_e32 v229, 0x40135761, v229
	v_mul_f32_e32 v230, 0x40135761, v230
	v_mul_f32_e32 v231, 0x40135761, v231
	v_exp_f32_e32 v228, v228
	v_exp_f32_e32 v229, v229
	v_exp_f32_e32 v230, v230
	v_exp_f32_e32 v231, v231
	v_add_u32_e32 v252, 0x3000, v252
	v_add_f32_e32 v228, 1.0, v228
	v_add_f32_e32 v229, 1.0, v229
	v_add_f32_e32 v230, 1.0, v230
	v_add_f32_e32 v231, 1.0, v231
	v_rcp_f32_e32 v228, v228
	v_rcp_f32_e32 v229, v229
	v_rcp_f32_e32 v230, v230
	v_rcp_f32_e32 v231, v231
	v_add_u32_e32 v252, v252, v15
	v_sub_f32_e32 v228, 1.0, v228
	v_sub_f32_e32 v229, 1.0, v229
	v_sub_f32_e32 v230, 1.0, v230
	v_sub_f32_e32 v231, 1.0, v231
	v_mul_f32_e32 v228, v228, v248
	v_mul_f32_e32 v229, v229, v249
	v_mul_f32_e32 v230, v230, v250
	v_mul_f32_e32 v231, v231, v251
	v_mul_f32_e32 v228, v142, v228
	v_mul_f32_e32 v229, v143, v229
	v_mul_f32_e32 v230, v144, v230
	v_mul_f32_e32 v231, v145, v231
	v_cvt_pk_bf16_f32 v142, v228, v229
	v_cvt_pk_bf16_f32 v143, v230, v231
	global_store_dwordx2 v252, v[142:143], s[54:55]
	s_waitcnt vmcnt(25)
	v_lshlrev_b32_e32 v248, 16, v98
	v_and_b32_e32 v249, 0xffff0000, v98
	v_lshlrev_b32_e32 v250, 16, v99
	v_and_b32_e32 v251, 0xffff0000, v99
	v_fma_f32 v44, v44, v40, v248
	v_fma_f32 v45, v45, v41, v249
	v_fma_f32 v46, v46, v42, v250
	v_fma_f32 v47, v47, v43, v251
	v_cmp_lt_u32_e32 vcc, 7, v6
	v_add_f32_e32 v146, v44, v146
	v_add_f32_e32 v147, v45, v147
	v_add_f32_e32 v148, v46, v148
	v_add_f32_e32 v149, v47, v149
	v_cndmask_b32_e32 v252, v12, v11, vcc
	v_lshlrev_b32_e32 v248, 16, v200
	v_and_b32_e32 v249, 0xffff0000, v200
	v_lshlrev_b32_e32 v250, 16, v201
	v_and_b32_e32 v251, 0xffff0000, v201
	v_mul_f32_e32 v228, 0x3d372713, v248
	v_mul_f32_e32 v229, 0x3d372713, v249
	v_mul_f32_e32 v230, 0x3d372713, v250
	v_mul_f32_e32 v231, 0x3d372713, v251
	v_mul_f32_e32 v228, v228, v248
	v_mul_f32_e32 v229, v229, v249
	v_mul_f32_e32 v230, v230, v250
	v_mul_f32_e32 v231, v231, v251
	v_fma_f32 v228, v228, v248, v248
	v_fma_f32 v229, v229, v249, v249
	v_fma_f32 v230, v230, v250, v250
	v_fma_f32 v231, v231, v251, v251
	v_mul_f32_e32 v228, 0x40135761, v228
	v_mul_f32_e32 v229, 0x40135761, v229
	v_mul_f32_e32 v230, 0x40135761, v230
	v_mul_f32_e32 v231, 0x40135761, v231
	v_exp_f32_e32 v228, v228
	v_exp_f32_e32 v229, v229
	v_exp_f32_e32 v230, v230
	v_exp_f32_e32 v231, v231
	v_add_u32_e32 v252, 0x3800, v252
	v_add_f32_e32 v228, 1.0, v228
	v_add_f32_e32 v229, 1.0, v229
	v_add_f32_e32 v230, 1.0, v230
	v_add_f32_e32 v231, 1.0, v231
	v_rcp_f32_e32 v228, v228
	v_rcp_f32_e32 v229, v229
	v_rcp_f32_e32 v230, v230
	v_rcp_f32_e32 v231, v231
	v_add_u32_e32 v252, v252, v15
	v_sub_f32_e32 v228, 1.0, v228
	v_sub_f32_e32 v229, 1.0, v229
	v_sub_f32_e32 v230, 1.0, v230
	v_sub_f32_e32 v231, 1.0, v231
	v_mul_f32_e32 v228, v228, v248
	v_mul_f32_e32 v229, v229, v249
	v_mul_f32_e32 v230, v230, v250
	v_mul_f32_e32 v231, v231, v251
	v_mul_f32_e32 v228, v146, v228
	v_mul_f32_e32 v229, v147, v229
	v_mul_f32_e32 v230, v148, v230
	v_mul_f32_e32 v231, v149, v231
	v_cvt_pk_bf16_f32 v146, v228, v229
	v_cvt_pk_bf16_f32 v147, v230, v231
	global_store_dwordx2 v252, v[146:147], s[54:55]
	s_waitcnt vmcnt(23)
	v_lshlrev_b32_e32 v248, 16, v100
	v_and_b32_e32 v249, 0xffff0000, v100
	v_lshlrev_b32_e32 v250, 16, v101
	v_and_b32_e32 v251, 0xffff0000, v101
	v_fma_f32 v48, v48, v44, v248
	v_fma_f32 v49, v49, v45, v249
	v_fma_f32 v50, v50, v46, v250
	v_fma_f32 v51, v51, v47, v251
	v_cmp_lt_u32_e32 vcc, 8, v6
	v_add_f32_e32 v150, v48, v150
	v_add_f32_e32 v151, v49, v151
	v_add_f32_e32 v152, v50, v152
	v_add_f32_e32 v153, v51, v153
	v_cndmask_b32_e32 v252, v12, v11, vcc
	v_lshlrev_b32_e32 v248, 16, v202
	v_and_b32_e32 v249, 0xffff0000, v202
	v_lshlrev_b32_e32 v250, 16, v203
	v_and_b32_e32 v251, 0xffff0000, v203
	v_mul_f32_e32 v228, 0x3d372713, v248
	v_mul_f32_e32 v229, 0x3d372713, v249
	v_mul_f32_e32 v230, 0x3d372713, v250
	v_mul_f32_e32 v231, 0x3d372713, v251
	v_mul_f32_e32 v228, v228, v248
	v_mul_f32_e32 v229, v229, v249
	v_mul_f32_e32 v230, v230, v250
	v_mul_f32_e32 v231, v231, v251
	v_fma_f32 v228, v228, v248, v248
	v_fma_f32 v229, v229, v249, v249
	v_fma_f32 v230, v230, v250, v250
	v_fma_f32 v231, v231, v251, v251
	v_mul_f32_e32 v228, 0x40135761, v228
	v_mul_f32_e32 v229, 0x40135761, v229
	v_mul_f32_e32 v230, 0x40135761, v230
	v_mul_f32_e32 v231, 0x40135761, v231
	v_exp_f32_e32 v228, v228
	v_exp_f32_e32 v229, v229
	v_exp_f32_e32 v230, v230
	v_exp_f32_e32 v231, v231
	v_add_u32_e32 v252, 0x4000, v252
	v_add_f32_e32 v228, 1.0, v228
	v_add_f32_e32 v229, 1.0, v229
	v_add_f32_e32 v230, 1.0, v230
	v_add_f32_e32 v231, 1.0, v231
	v_rcp_f32_e32 v228, v228
	v_rcp_f32_e32 v229, v229
	v_rcp_f32_e32 v230, v230
	v_rcp_f32_e32 v231, v231
	v_add_u32_e32 v252, v252, v15
	v_sub_f32_e32 v228, 1.0, v228
	v_sub_f32_e32 v229, 1.0, v229
	v_sub_f32_e32 v230, 1.0, v230
	v_sub_f32_e32 v231, 1.0, v231
	v_mul_f32_e32 v228, v228, v248
	v_mul_f32_e32 v229, v229, v249
	v_mul_f32_e32 v230, v230, v250
	v_mul_f32_e32 v231, v231, v251
	v_mul_f32_e32 v228, v150, v228
	v_mul_f32_e32 v229, v151, v229
	v_mul_f32_e32 v230, v152, v230
	v_mul_f32_e32 v231, v153, v231
	v_cvt_pk_bf16_f32 v150, v228, v229
	v_cvt_pk_bf16_f32 v151, v230, v231
	global_store_dwordx2 v252, v[150:151], s[54:55]
	s_waitcnt vmcnt(23)
	v_lshlrev_b32_e32 v248, 16, v102
	v_and_b32_e32 v249, 0xffff0000, v102
	v_lshlrev_b32_e32 v250, 16, v103
	v_and_b32_e32 v251, 0xffff0000, v103
	v_fma_f32 v52, v52, v48, v248
	v_fma_f32 v53, v53, v49, v249
	v_fma_f32 v54, v54, v50, v250
	v_fma_f32 v55, v55, v51, v251
	v_cmp_lt_u32_e32 vcc, 9, v6
	v_add_f32_e32 v154, v52, v154
	v_add_f32_e32 v155, v53, v155
	v_add_f32_e32 v156, v54, v156
	v_add_f32_e32 v157, v55, v157
	v_cndmask_b32_e32 v252, v12, v11, vcc
	v_lshlrev_b32_e32 v248, 16, v204
	v_and_b32_e32 v249, 0xffff0000, v204
	v_lshlrev_b32_e32 v250, 16, v205
	v_and_b32_e32 v251, 0xffff0000, v205
	v_mul_f32_e32 v228, 0x3d372713, v248
	v_mul_f32_e32 v229, 0x3d372713, v249
	v_mul_f32_e32 v230, 0x3d372713, v250
	v_mul_f32_e32 v231, 0x3d372713, v251
	v_mul_f32_e32 v228, v228, v248
	v_mul_f32_e32 v229, v229, v249
	v_mul_f32_e32 v230, v230, v250
	v_mul_f32_e32 v231, v231, v251
	v_fma_f32 v228, v228, v248, v248
	v_fma_f32 v229, v229, v249, v249
	v_fma_f32 v230, v230, v250, v250
	v_fma_f32 v231, v231, v251, v251
	v_mul_f32_e32 v228, 0x40135761, v228
	v_mul_f32_e32 v229, 0x40135761, v229
	v_mul_f32_e32 v230, 0x40135761, v230
	v_mul_f32_e32 v231, 0x40135761, v231
	v_exp_f32_e32 v228, v228
	v_exp_f32_e32 v229, v229
	v_exp_f32_e32 v230, v230
	v_exp_f32_e32 v231, v231
	v_add_u32_e32 v252, 0x4800, v252
	v_add_f32_e32 v228, 1.0, v228
	v_add_f32_e32 v229, 1.0, v229
	v_add_f32_e32 v230, 1.0, v230
	v_add_f32_e32 v231, 1.0, v231
	v_rcp_f32_e32 v228, v228
	v_rcp_f32_e32 v229, v229
	v_rcp_f32_e32 v230, v230
	v_rcp_f32_e32 v231, v231
	v_add_u32_e32 v252, v252, v15
	v_sub_f32_e32 v228, 1.0, v228
	v_sub_f32_e32 v229, 1.0, v229
	v_sub_f32_e32 v230, 1.0, v230
	v_sub_f32_e32 v231, 1.0, v231
	v_mul_f32_e32 v228, v228, v248
	v_mul_f32_e32 v229, v229, v249
	v_mul_f32_e32 v230, v230, v250
	v_mul_f32_e32 v231, v231, v251
	v_mul_f32_e32 v228, v154, v228
	v_mul_f32_e32 v229, v155, v229
	v_mul_f32_e32 v230, v156, v230
	v_mul_f32_e32 v231, v157, v231
	v_cvt_pk_bf16_f32 v154, v228, v229
	v_cvt_pk_bf16_f32 v155, v230, v231
	global_store_dwordx2 v252, v[154:155], s[54:55]
	s_waitcnt vmcnt(21)
	v_lshlrev_b32_e32 v248, 16, v104
	v_and_b32_e32 v249, 0xffff0000, v104
	v_lshlrev_b32_e32 v250, 16, v105
	v_and_b32_e32 v251, 0xffff0000, v105
	v_fma_f32 v56, v56, v52, v248
	v_fma_f32 v57, v57, v53, v249
	v_fma_f32 v58, v58, v54, v250
	v_fma_f32 v59, v59, v55, v251
	v_cmp_lt_u32_e32 vcc, 10, v6
	v_add_f32_e32 v158, v56, v158
	v_add_f32_e32 v159, v57, v159
	v_add_f32_e32 v160, v58, v160
	v_add_f32_e32 v161, v59, v161
	v_cndmask_b32_e32 v252, v12, v11, vcc
	v_lshlrev_b32_e32 v248, 16, v206
	v_and_b32_e32 v249, 0xffff0000, v206
	v_lshlrev_b32_e32 v250, 16, v207
	v_and_b32_e32 v251, 0xffff0000, v207
	v_mul_f32_e32 v228, 0x3d372713, v248
	v_mul_f32_e32 v229, 0x3d372713, v249
	v_mul_f32_e32 v230, 0x3d372713, v250
	v_mul_f32_e32 v231, 0x3d372713, v251
	v_mul_f32_e32 v228, v228, v248
	v_mul_f32_e32 v229, v229, v249
	v_mul_f32_e32 v230, v230, v250
	v_mul_f32_e32 v231, v231, v251
	v_fma_f32 v228, v228, v248, v248
	v_fma_f32 v229, v229, v249, v249
	v_fma_f32 v230, v230, v250, v250
	v_fma_f32 v231, v231, v251, v251
	v_mul_f32_e32 v228, 0x40135761, v228
	v_mul_f32_e32 v229, 0x40135761, v229
	v_mul_f32_e32 v230, 0x40135761, v230
	v_mul_f32_e32 v231, 0x40135761, v231
	v_exp_f32_e32 v228, v228
	v_exp_f32_e32 v229, v229
	v_exp_f32_e32 v230, v230
	v_exp_f32_e32 v231, v231
	v_add_u32_e32 v252, 0x5000, v252
	v_add_f32_e32 v228, 1.0, v228
	v_add_f32_e32 v229, 1.0, v229
	v_add_f32_e32 v230, 1.0, v230
	v_add_f32_e32 v231, 1.0, v231
	v_rcp_f32_e32 v228, v228
	v_rcp_f32_e32 v229, v229
	v_rcp_f32_e32 v230, v230
	v_rcp_f32_e32 v231, v231
	v_add_u32_e32 v252, v252, v15
	v_sub_f32_e32 v228, 1.0, v228
	v_sub_f32_e32 v229, 1.0, v229
	v_sub_f32_e32 v230, 1.0, v230
	v_sub_f32_e32 v231, 1.0, v231
	v_mul_f32_e32 v228, v228, v248
	v_mul_f32_e32 v229, v229, v249
	v_mul_f32_e32 v230, v230, v250
	v_mul_f32_e32 v231, v231, v251
	v_mul_f32_e32 v228, v158, v228
	v_mul_f32_e32 v229, v159, v229
	v_mul_f32_e32 v230, v160, v230
	v_mul_f32_e32 v231, v161, v231
	v_cvt_pk_bf16_f32 v158, v228, v229
	v_cvt_pk_bf16_f32 v159, v230, v231
	global_store_dwordx2 v252, v[158:159], s[54:55]
	s_waitcnt vmcnt(21)
	v_lshlrev_b32_e32 v248, 16, v106
	v_and_b32_e32 v249, 0xffff0000, v106
	v_lshlrev_b32_e32 v250, 16, v107
	v_and_b32_e32 v251, 0xffff0000, v107
	v_fma_f32 v60, v60, v56, v248
	v_fma_f32 v61, v61, v57, v249
	v_fma_f32 v62, v62, v58, v250
	v_fma_f32 v63, v63, v59, v251
	v_cmp_lt_u32_e32 vcc, 11, v6
	v_add_f32_e32 v162, v60, v162
	v_add_f32_e32 v163, v61, v163
	v_add_f32_e32 v164, v62, v164
	v_add_f32_e32 v165, v63, v165
	v_cndmask_b32_e32 v252, v12, v11, vcc
	v_lshlrev_b32_e32 v248, 16, v208
	v_and_b32_e32 v249, 0xffff0000, v208
	v_lshlrev_b32_e32 v250, 16, v209
	v_and_b32_e32 v251, 0xffff0000, v209
	v_mul_f32_e32 v228, 0x3d372713, v248
	v_mul_f32_e32 v229, 0x3d372713, v249
	v_mul_f32_e32 v230, 0x3d372713, v250
	v_mul_f32_e32 v231, 0x3d372713, v251
	v_mul_f32_e32 v228, v228, v248
	v_mul_f32_e32 v229, v229, v249
	v_mul_f32_e32 v230, v230, v250
	v_mul_f32_e32 v231, v231, v251
	v_fma_f32 v228, v228, v248, v248
	v_fma_f32 v229, v229, v249, v249
	v_fma_f32 v230, v230, v250, v250
	v_fma_f32 v231, v231, v251, v251
	v_mul_f32_e32 v228, 0x40135761, v228
	v_mul_f32_e32 v229, 0x40135761, v229
	v_mul_f32_e32 v230, 0x40135761, v230
	v_mul_f32_e32 v231, 0x40135761, v231
	v_exp_f32_e32 v228, v228
	v_exp_f32_e32 v229, v229
	v_exp_f32_e32 v230, v230
	v_exp_f32_e32 v231, v231
	v_add_u32_e32 v252, 0x5800, v252
	v_add_f32_e32 v228, 1.0, v228
	v_add_f32_e32 v229, 1.0, v229
	v_add_f32_e32 v230, 1.0, v230
	v_add_f32_e32 v231, 1.0, v231
	v_rcp_f32_e32 v228, v228
	v_rcp_f32_e32 v229, v229
	v_rcp_f32_e32 v230, v230
	v_rcp_f32_e32 v231, v231
	v_add_u32_e32 v252, v252, v15
	v_sub_f32_e32 v228, 1.0, v228
	v_sub_f32_e32 v229, 1.0, v229
	v_sub_f32_e32 v230, 1.0, v230
	v_sub_f32_e32 v231, 1.0, v231
	v_mul_f32_e32 v228, v228, v248
	v_mul_f32_e32 v229, v229, v249
	v_mul_f32_e32 v230, v230, v250
	v_mul_f32_e32 v231, v231, v251
	v_mul_f32_e32 v228, v162, v228
	v_mul_f32_e32 v229, v163, v229
	v_mul_f32_e32 v230, v164, v230
	v_mul_f32_e32 v231, v165, v231
	v_cvt_pk_bf16_f32 v162, v228, v229
	v_cvt_pk_bf16_f32 v163, v230, v231
	global_store_dwordx2 v252, v[162:163], s[54:55]
	s_waitcnt vmcnt(19)
	v_lshlrev_b32_e32 v248, 16, v108
	v_and_b32_e32 v249, 0xffff0000, v108
	v_lshlrev_b32_e32 v250, 16, v109
	v_and_b32_e32 v251, 0xffff0000, v109
	v_fma_f32 v64, v64, v60, v248
	v_fma_f32 v65, v65, v61, v249
	v_fma_f32 v66, v66, v62, v250
	v_fma_f32 v67, v67, v63, v251
	v_cmp_lt_u32_e32 vcc, 12, v6
	v_add_f32_e32 v166, v64, v166
	v_add_f32_e32 v167, v65, v167
	v_add_f32_e32 v168, v66, v168
	v_add_f32_e32 v169, v67, v169
	v_cndmask_b32_e32 v252, v12, v11, vcc
	v_lshlrev_b32_e32 v248, 16, v210
	v_and_b32_e32 v249, 0xffff0000, v210
	v_lshlrev_b32_e32 v250, 16, v211
	v_and_b32_e32 v251, 0xffff0000, v211
	v_mul_f32_e32 v228, 0x3d372713, v248
	v_mul_f32_e32 v229, 0x3d372713, v249
	v_mul_f32_e32 v230, 0x3d372713, v250
	v_mul_f32_e32 v231, 0x3d372713, v251
	v_mul_f32_e32 v228, v228, v248
	v_mul_f32_e32 v229, v229, v249
	v_mul_f32_e32 v230, v230, v250
	v_mul_f32_e32 v231, v231, v251
	v_fma_f32 v228, v228, v248, v248
	v_fma_f32 v229, v229, v249, v249
	v_fma_f32 v230, v230, v250, v250
	v_fma_f32 v231, v231, v251, v251
	v_mul_f32_e32 v228, 0x40135761, v228
	v_mul_f32_e32 v229, 0x40135761, v229
	v_mul_f32_e32 v230, 0x40135761, v230
	v_mul_f32_e32 v231, 0x40135761, v231
	v_exp_f32_e32 v228, v228
	v_exp_f32_e32 v229, v229
	v_exp_f32_e32 v230, v230
	v_exp_f32_e32 v231, v231
	v_add_u32_e32 v252, 0x6000, v252
	v_add_f32_e32 v228, 1.0, v228
	v_add_f32_e32 v229, 1.0, v229
	v_add_f32_e32 v230, 1.0, v230
	v_add_f32_e32 v231, 1.0, v231
	v_rcp_f32_e32 v228, v228
	v_rcp_f32_e32 v229, v229
	v_rcp_f32_e32 v230, v230
	v_rcp_f32_e32 v231, v231
	v_add_u32_e32 v252, v252, v15
	v_sub_f32_e32 v228, 1.0, v228
	v_sub_f32_e32 v229, 1.0, v229
	v_sub_f32_e32 v230, 1.0, v230
	v_sub_f32_e32 v231, 1.0, v231
	v_mul_f32_e32 v228, v228, v248
	v_mul_f32_e32 v229, v229, v249
	v_mul_f32_e32 v230, v230, v250
	v_mul_f32_e32 v231, v231, v251
	v_mul_f32_e32 v228, v166, v228
	v_mul_f32_e32 v229, v167, v229
	v_mul_f32_e32 v230, v168, v230
	v_mul_f32_e32 v231, v169, v231
	v_cvt_pk_bf16_f32 v166, v228, v229
	v_cvt_pk_bf16_f32 v167, v230, v231
	global_store_dwordx2 v252, v[166:167], s[54:55]
	s_waitcnt vmcnt(19)
	v_lshlrev_b32_e32 v248, 16, v110
	v_and_b32_e32 v249, 0xffff0000, v110
	v_lshlrev_b32_e32 v250, 16, v111
	v_and_b32_e32 v251, 0xffff0000, v111
	v_fma_f32 v68, v68, v64, v248
	v_fma_f32 v69, v69, v65, v249
	v_fma_f32 v70, v70, v66, v250
	v_fma_f32 v71, v71, v67, v251
	v_cmp_lt_u32_e32 vcc, 13, v6
	v_add_f32_e32 v170, v68, v170
	v_add_f32_e32 v171, v69, v171
	v_add_f32_e32 v172, v70, v172
	v_add_f32_e32 v173, v71, v173
	v_cndmask_b32_e32 v252, v12, v11, vcc
	v_lshlrev_b32_e32 v248, 16, v212
	v_and_b32_e32 v249, 0xffff0000, v212
	v_lshlrev_b32_e32 v250, 16, v213
	v_and_b32_e32 v251, 0xffff0000, v213
	v_mul_f32_e32 v228, 0x3d372713, v248
	v_mul_f32_e32 v229, 0x3d372713, v249
	v_mul_f32_e32 v230, 0x3d372713, v250
	v_mul_f32_e32 v231, 0x3d372713, v251
	v_mul_f32_e32 v228, v228, v248
	v_mul_f32_e32 v229, v229, v249
	v_mul_f32_e32 v230, v230, v250
	v_mul_f32_e32 v231, v231, v251
	v_fma_f32 v228, v228, v248, v248
	v_fma_f32 v229, v229, v249, v249
	v_fma_f32 v230, v230, v250, v250
	v_fma_f32 v231, v231, v251, v251
	v_mul_f32_e32 v228, 0x40135761, v228
	v_mul_f32_e32 v229, 0x40135761, v229
	v_mul_f32_e32 v230, 0x40135761, v230
	v_mul_f32_e32 v231, 0x40135761, v231
	v_exp_f32_e32 v228, v228
	v_exp_f32_e32 v229, v229
	v_exp_f32_e32 v230, v230
	v_exp_f32_e32 v231, v231
	v_add_u32_e32 v252, 0x6800, v252
	v_add_f32_e32 v228, 1.0, v228
	v_add_f32_e32 v229, 1.0, v229
	v_add_f32_e32 v230, 1.0, v230
	v_add_f32_e32 v231, 1.0, v231
	v_rcp_f32_e32 v228, v228
	v_rcp_f32_e32 v229, v229
	v_rcp_f32_e32 v230, v230
	v_rcp_f32_e32 v231, v231
	v_add_u32_e32 v252, v252, v15
	v_sub_f32_e32 v228, 1.0, v228
	v_sub_f32_e32 v229, 1.0, v229
	v_sub_f32_e32 v230, 1.0, v230
	v_sub_f32_e32 v231, 1.0, v231
	v_mul_f32_e32 v228, v228, v248
	v_mul_f32_e32 v229, v229, v249
	v_mul_f32_e32 v230, v230, v250
	v_mul_f32_e32 v231, v231, v251
	v_mul_f32_e32 v228, v170, v228
	v_mul_f32_e32 v229, v171, v229
	v_mul_f32_e32 v230, v172, v230
	v_mul_f32_e32 v231, v173, v231
	v_cvt_pk_bf16_f32 v170, v228, v229
	v_cvt_pk_bf16_f32 v171, v230, v231
	global_store_dwordx2 v252, v[170:171], s[54:55]
	s_waitcnt vmcnt(17)
	v_lshlrev_b32_e32 v248, 16, v112
	v_and_b32_e32 v249, 0xffff0000, v112
	v_lshlrev_b32_e32 v250, 16, v113
	v_and_b32_e32 v251, 0xffff0000, v113
	v_fma_f32 v72, v72, v68, v248
	v_fma_f32 v73, v73, v69, v249
	v_fma_f32 v74, v74, v70, v250
	v_fma_f32 v75, v75, v71, v251
	v_cmp_lt_u32_e32 vcc, 14, v6
	v_add_f32_e32 v174, v72, v174
	v_add_f32_e32 v175, v73, v175
	v_add_f32_e32 v176, v74, v176
	v_add_f32_e32 v177, v75, v177
	v_cndmask_b32_e32 v252, v12, v11, vcc
	v_lshlrev_b32_e32 v248, 16, v214
	v_and_b32_e32 v249, 0xffff0000, v214
	v_lshlrev_b32_e32 v250, 16, v215
	v_and_b32_e32 v251, 0xffff0000, v215
	v_mul_f32_e32 v228, 0x3d372713, v248
	v_mul_f32_e32 v229, 0x3d372713, v249
	v_mul_f32_e32 v230, 0x3d372713, v250
	v_mul_f32_e32 v231, 0x3d372713, v251
	v_mul_f32_e32 v228, v228, v248
	v_mul_f32_e32 v229, v229, v249
	v_mul_f32_e32 v230, v230, v250
	v_mul_f32_e32 v231, v231, v251
	v_fma_f32 v228, v228, v248, v248
	v_fma_f32 v229, v229, v249, v249
	v_fma_f32 v230, v230, v250, v250
	v_fma_f32 v231, v231, v251, v251
	v_mul_f32_e32 v228, 0x40135761, v228
	v_mul_f32_e32 v229, 0x40135761, v229
	v_mul_f32_e32 v230, 0x40135761, v230
	v_mul_f32_e32 v231, 0x40135761, v231
	v_exp_f32_e32 v228, v228
	v_exp_f32_e32 v229, v229
	v_exp_f32_e32 v230, v230
	v_exp_f32_e32 v231, v231
	v_add_u32_e32 v252, 0x7000, v252
	v_add_f32_e32 v228, 1.0, v228
	v_add_f32_e32 v229, 1.0, v229
	v_add_f32_e32 v230, 1.0, v230
	v_add_f32_e32 v231, 1.0, v231
	v_rcp_f32_e32 v228, v228
	v_rcp_f32_e32 v229, v229
	v_rcp_f32_e32 v230, v230
	v_rcp_f32_e32 v231, v231
	v_add_u32_e32 v252, v252, v15
	v_sub_f32_e32 v228, 1.0, v228
	v_sub_f32_e32 v229, 1.0, v229
	v_sub_f32_e32 v230, 1.0, v230
	v_sub_f32_e32 v231, 1.0, v231
	v_mul_f32_e32 v228, v228, v248
	v_mul_f32_e32 v229, v229, v249
	v_mul_f32_e32 v230, v230, v250
	v_mul_f32_e32 v231, v231, v251
	v_mul_f32_e32 v228, v174, v228
	v_mul_f32_e32 v229, v175, v229
	v_mul_f32_e32 v230, v176, v230
	v_mul_f32_e32 v231, v177, v231
	v_cvt_pk_bf16_f32 v174, v228, v229
	v_cvt_pk_bf16_f32 v175, v230, v231
	global_store_dwordx2 v252, v[174:175], s[54:55]
	s_waitcnt vmcnt(17)
	v_lshlrev_b32_e32 v248, 16, v114
	v_and_b32_e32 v249, 0xffff0000, v114
	v_lshlrev_b32_e32 v250, 16, v115
	v_and_b32_e32 v251, 0xffff0000, v115
	v_fma_f32 v76, v76, v72, v248
	v_fma_f32 v77, v77, v73, v249
	v_fma_f32 v78, v78, v74, v250
	v_fma_f32 v79, v79, v75, v251
	v_cmp_lt_u32_e32 vcc, 15, v6
	v_add_f32_e32 v178, v76, v178
	v_add_f32_e32 v179, v77, v179
	v_add_f32_e32 v180, v78, v180
	v_add_f32_e32 v181, v79, v181
	v_cndmask_b32_e32 v252, v12, v11, vcc
	v_lshlrev_b32_e32 v248, 16, v216
	v_and_b32_e32 v249, 0xffff0000, v216
	v_lshlrev_b32_e32 v250, 16, v217
	v_and_b32_e32 v251, 0xffff0000, v217
	v_mul_f32_e32 v228, 0x3d372713, v248
	v_mul_f32_e32 v229, 0x3d372713, v249
	v_mul_f32_e32 v230, 0x3d372713, v250
	v_mul_f32_e32 v231, 0x3d372713, v251
	v_mul_f32_e32 v228, v228, v248
	v_mul_f32_e32 v229, v229, v249
	v_mul_f32_e32 v230, v230, v250
	v_mul_f32_e32 v231, v231, v251
	v_fma_f32 v228, v228, v248, v248
	v_fma_f32 v229, v229, v249, v249
	v_fma_f32 v230, v230, v250, v250
	v_fma_f32 v231, v231, v251, v251
	v_mul_f32_e32 v228, 0x40135761, v228
	v_mul_f32_e32 v229, 0x40135761, v229
	v_mul_f32_e32 v230, 0x40135761, v230
	v_mul_f32_e32 v231, 0x40135761, v231
	v_exp_f32_e32 v228, v228
	v_exp_f32_e32 v229, v229
	v_exp_f32_e32 v230, v230
	v_exp_f32_e32 v231, v231
	v_add_u32_e32 v252, 0x7800, v252
	v_add_f32_e32 v228, 1.0, v228
	v_add_f32_e32 v229, 1.0, v229
	v_add_f32_e32 v230, 1.0, v230
	v_add_f32_e32 v231, 1.0, v231
	v_rcp_f32_e32 v228, v228
	v_rcp_f32_e32 v229, v229
	v_rcp_f32_e32 v230, v230
	v_rcp_f32_e32 v231, v231
	v_add_u32_e32 v252, v252, v15
	v_sub_f32_e32 v228, 1.0, v228
	v_sub_f32_e32 v229, 1.0, v229
	v_sub_f32_e32 v230, 1.0, v230
	v_sub_f32_e32 v231, 1.0, v231
	v_mul_f32_e32 v228, v228, v248
	v_mul_f32_e32 v229, v229, v249
	v_mul_f32_e32 v230, v230, v250
	v_mul_f32_e32 v231, v231, v251
	v_mul_f32_e32 v228, v178, v228
	v_mul_f32_e32 v229, v179, v229
	v_mul_f32_e32 v230, v180, v230
	v_mul_f32_e32 v231, v181, v231
	v_cvt_pk_bf16_f32 v178, v228, v229
	v_cvt_pk_bf16_f32 v179, v230, v231
	global_store_dwordx2 v252, v[178:179], s[54:55]
	s_waitcnt vmcnt(16)
	v_lshlrev_b32_e32 v248, 16, v116
	v_and_b32_e32 v249, 0xffff0000, v116
	v_lshlrev_b32_e32 v250, 16, v117
	v_and_b32_e32 v251, 0xffff0000, v117
	v_fma_f32 v80, v80, v76, v248
	v_fma_f32 v81, v81, v77, v249
	v_fma_f32 v82, v82, v78, v250
	v_fma_f32 v83, v83, v79, v251
	v_cmp_lt_u32_e32 vcc, 16, v6
	v_add_f32_e32 v182, v80, v182
	v_add_f32_e32 v183, v81, v183
	v_add_f32_e32 v184, v82, v184
	v_add_f32_e32 v185, v83, v185
	v_cndmask_b32_e32 v252, v12, v11, vcc
	v_lshlrev_b32_e32 v248, 16, v218
	v_and_b32_e32 v249, 0xffff0000, v218
	v_lshlrev_b32_e32 v250, 16, v219
	v_and_b32_e32 v251, 0xffff0000, v219
	v_mul_f32_e32 v228, 0x3d372713, v248
	v_mul_f32_e32 v229, 0x3d372713, v249
	v_mul_f32_e32 v230, 0x3d372713, v250
	v_mul_f32_e32 v231, 0x3d372713, v251
	v_mul_f32_e32 v228, v228, v248
	v_mul_f32_e32 v229, v229, v249
	v_mul_f32_e32 v230, v230, v250
	v_mul_f32_e32 v231, v231, v251
	v_fma_f32 v228, v228, v248, v248
	v_fma_f32 v229, v229, v249, v249
	v_fma_f32 v230, v230, v250, v250
	v_fma_f32 v231, v231, v251, v251
	v_mul_f32_e32 v228, 0x40135761, v228
	v_mul_f32_e32 v229, 0x40135761, v229
	v_mul_f32_e32 v230, 0x40135761, v230
	v_mul_f32_e32 v231, 0x40135761, v231
	v_exp_f32_e32 v228, v228
	v_exp_f32_e32 v229, v229
	v_exp_f32_e32 v230, v230
	v_exp_f32_e32 v231, v231
	v_add_u32_e32 v252, 0x8000, v252
	v_add_f32_e32 v228, 1.0, v228
	v_add_f32_e32 v229, 1.0, v229
	v_add_f32_e32 v230, 1.0, v230
	v_add_f32_e32 v231, 1.0, v231
	v_rcp_f32_e32 v228, v228
	v_rcp_f32_e32 v229, v229
	v_rcp_f32_e32 v230, v230
	v_rcp_f32_e32 v231, v231
	v_add_u32_e32 v252, v252, v15
	v_sub_f32_e32 v228, 1.0, v228
	v_sub_f32_e32 v229, 1.0, v229
	v_sub_f32_e32 v230, 1.0, v230
	v_sub_f32_e32 v231, 1.0, v231
	v_mul_f32_e32 v228, v228, v248
	v_mul_f32_e32 v229, v229, v249
	v_mul_f32_e32 v230, v230, v250
	v_mul_f32_e32 v231, v231, v251
	v_mul_f32_e32 v228, v182, v228
	v_mul_f32_e32 v229, v183, v229
	v_mul_f32_e32 v230, v184, v230
	v_mul_f32_e32 v231, v185, v231
	v_cvt_pk_bf16_f32 v182, v228, v229
	v_cvt_pk_bf16_f32 v183, v230, v231
	global_store_dwordx2 v252, v[182:183], s[54:55]
	s_waitcnt vmcnt(0)
	s_barrier
